# baseline (speedup 1.0000x reference)
.LBB0_14:
	s_waitcnt lgkmcnt(0)
	s_ashr_i32 s0, s14, 31
	s_lshr_b32 s0, s0, 26
	s_add_i32 s0, s14, s0
	s_ashr_i32 s0, s0, 6
	s_abs_i32 s1, s0
	v_cvt_f32_u32_e32 v1, s1
	s_sub_i32 s7, 0, s1
	s_sub_i32 s2, s2, s16
	s_abs_i32 s3, s2
	v_rcp_iflag_f32_e32 v1, v1
	s_xor_b32 s6, s2, s0
	s_ashr_i32 s6, s6, 31
	v_and_b32_e32 v26, 15, v0
	v_mul_f32_e32 v1, 0x4f7ffffe, v1
	v_cvt_u32_f32_e32 v1, v1
	v_lshrrev_b32_e32 v20, 4, v0
	v_lshlrev_b32_e32 v16, 4, v26
	v_mov_b32_e32 v17, 0
	v_readfirstlane_b32 s10, v1
	s_mul_i32 s7, s7, s10
	s_mul_hi_u32 s7, s10, s7
	s_add_i32 s10, s10, s7
	s_mul_hi_u32 s7, s3, s10
	s_mul_i32 s10, s7, s1
	s_sub_i32 s3, s3, s10
	s_add_i32 s11, s7, 1
	s_sub_i32 s10, s3, s1
	s_cmp_ge_u32 s3, s1
	s_cselect_b32 s7, s11, s7
	s_cselect_b32 s3, s10, s3
	s_add_i32 s10, s7, 1
	s_cmp_ge_u32 s3, s1
	s_cselect_b32 s1, s10, s7
	s_xor_b32 s1, s1, s6
	s_sub_i32 s1, s1, s6
	s_mul_i32 s3, s1, s0
	s_lshl_b32 s0, s1, 6
	s_sub_i32 s1, s2, s3
	s_lshl_b32 s2, s1, 6
	s_ashr_i32 s3, s2, 31
	s_lshl_b64 s[6:7], s[2:3], 2
	s_add_u32 s6, s8, s6
	v_or_b32_e32 v2, s0, v20
	s_addc_u32 s7, s9, s7
	v_lshl_add_u64 v[12:13], s[6:7], 0, v[16:17]
	v_mad_i64_i32 v[0:1], s[6:7], v2, s14, 0
	v_lshl_add_u64 v[8:9], v[0:1], 2, v[12:13]
	v_or_b32_e32 v0, 16, v2
	v_mad_i64_i32 v[0:1], s[6:7], v0, s14, 0
	v_lshl_add_u64 v[10:11], v[0:1], 2, v[12:13]
	v_or_b32_e32 v0, 32, v2
	v_mad_i64_i32 v[0:1], s[6:7], v0, s14, 0
	v_lshl_add_u64 v[14:15], v[0:1], 2, v[12:13]
	v_or_b32_e32 v18, 48, v2
	global_load_dwordx4 v[0:3], v[8:9], off
	global_load_dwordx4 v[4:7], v[10:11], off
	v_mad_i64_i32 v[18:19], s[6:7], v18, s14, 0
	global_load_dwordx4 v[8:11], v[14:15], off
	v_lshl_add_u64 v[12:13], v[18:19], 2, v[12:13]
	global_load_dwordx4 v[12:15], v[12:13], off
	s_movk_i32 s1, 0x104
	s_movk_i32 s3, 0x410
	v_lshlrev_b32_e32 v18, 2, v20
	v_mad_u32_u24 v27, v20, s1, v16
	v_mad_u32_u24 v28, v26, s3, v18
	s_ashr_i32 s1, s0, 31
	v_add_u32_e32 v29, 0x1040, v27
	v_add_u32_e32 v30, 0x1048, v27
	v_add_u32_e32 v31, 0x2080, v27
	v_add_u32_e32 v32, 0x2088, v27
	v_add_u32_e32 v33, 0x30c0, v27
	v_add_u32_e32 v34, 0x30c8, v27
	v_or_b32_e32 v16, s2, v20
	s_lshl_b64 s[0:1], s[0:1], 1
	v_mad_i64_i32 v[18:19], s[2:3], v16, s12, 0
	v_or_b32_e32 v20, 16, v16
	v_or_b32_e32 v22, 32, v16
	v_or_b32_e32 v16, 48, v16
	s_add_u32 s0, s4, s0
	v_mad_i64_i32 v[24:25], s[2:3], v16, s12, 0
	v_lshlrev_b32_e32 v16, 3, v26
	s_addc_u32 s1, s5, s1
	v_mad_i64_i32 v[20:21], s[2:3], v20, s12, 0
	v_mad_i64_i32 v[22:23], s[2:3], v22, s12, 0
	v_lshl_add_u64 v[16:17], s[0:1], 0, v[16:17]
	v_lshl_add_u64 v[18:19], v[18:19], 1, v[16:17]
	v_lshl_add_u64 v[20:21], v[20:21], 1, v[16:17]
	v_lshl_add_u64 v[22:23], v[22:23], 1, v[16:17]
	v_lshl_add_u64 v[16:17], v[24:25], 1, v[16:17]
	s_waitcnt vmcnt(3)
	ds_write2_b32 v27, v0, v1 offset1:1
	ds_write2_b32 v27, v2, v3 offset0:2 offset1:3
	s_waitcnt vmcnt(2)
	ds_write2_b32 v29, v4, v5 offset1:1
	ds_write2_b32 v30, v6, v7 offset1:1
	s_waitcnt vmcnt(1)
	ds_write2_b32 v31, v8, v9 offset1:1
	ds_write2_b32 v32, v10, v11 offset1:1
	s_waitcnt vmcnt(0)
	ds_write2_b32 v33, v12, v13 offset1:1
	ds_write2_b32 v34, v14, v15 offset1:1
	s_waitcnt lgkmcnt(0)
	s_barrier
	ds_read2_b32 v[0:1], v28 offset1:16
	ds_read2_b32 v[2:3], v28 offset0:65 offset1:81
	ds_read2_b32 v[4:5], v28 offset0:130 offset1:146
	ds_read2_b32 v[6:7], v28 offset0:195 offset1:211
	ds_read2_b32 v[8:9], v28 offset0:32 offset1:48
	ds_read2_b32 v[10:11], v28 offset0:97 offset1:113
	ds_read2_b32 v[12:13], v28 offset0:162 offset1:178
	ds_read2_b32 v[14:15], v28 offset0:227 offset1:243
	s_waitcnt lgkmcnt(6)
	v_cvt_pk_bf16_f32 v24, v0, v2
	s_waitcnt lgkmcnt(4)
	v_cvt_pk_bf16_f32 v25, v4, v6
	v_cvt_pk_bf16_f32 v0, v1, v3
	v_cvt_pk_bf16_f32 v1, v5, v7
	s_waitcnt lgkmcnt(2)
	v_cvt_pk_bf16_f32 v2, v8, v10
	s_waitcnt lgkmcnt(0)
	v_cvt_pk_bf16_f32 v3, v12, v14
	v_cvt_pk_bf16_f32 v4, v9, v11
	v_cvt_pk_bf16_f32 v5, v13, v15
	global_store_dwordx2 v[18:19], v[24:25], off
	global_store_dwordx2 v[20:21], v[0:1], off
	global_store_dwordx2 v[22:23], v[2:3], off
	global_store_dwordx2 v[16:17], v[4:5], off
	s_barrier
	s_endpgm
	.p2align	8

.LBB2_23:
	s_endpgm
	.p2align	8

.LBB3_15:
	s_load_dwordx2 s[0:1], s[0:1], 0x20
	v_or_b32_e32 v0, s9, v151
	s_waitcnt lgkmcnt(0)
	v_lshl_add_u32 v66, v152, 6, v0
	v_ashrrev_i32_e32 v67, 31, v66
	v_lshlrev_b64 v[0:1], 6, v[66:67]
	v_lshl_add_u64 v[0:1], s[0:1], 0, v[0:1]
	global_load_dwordx4 v[68:71], v[0:1], off
	global_load_dwordx4 v[72:75], v[0:1], off offset:32
	global_load_dwordx4 v[76:79], v[0:1], off offset:16
	global_load_dwordx4 v[80:83], v[0:1], off offset:48
	v_mov_b32_e32 v67, 0x358637bd
	s_mov_b32 s4, 0xc0135761
	v_lshlrev_b32_e32 v0, 6, v150
	v_lshl_or_b32 v0, v149, 2, v0
	v_add_u32_e32 v0, s8, v0
	v_ashrrev_i32_e32 v1, 31, v0
	s_movk_i32 s5, 0x1800
	v_lshl_add_u64 v[0:1], v[0:1], 1, s[2:3]
	s_waitcnt vmcnt(0)
	v_mov_b32_e32 v84, v68
	v_mov_b32_e32 v85, v72
	v_mov_b32_e32 v72, v69
	v_mov_b32_e32 v68, v70
	v_mov_b32_e32 v69, v74
	v_mov_b32_e32 v74, v71
	v_mov_b32_e32 v70, v76
	v_mov_b32_e32 v71, v80
	v_mov_b32_e32 v80, v77
	v_mov_b32_e32 v76, v78
	v_mov_b32_e32 v77, v82
	v_mov_b32_e32 v82, v79
	v_pk_add_f32 v[72:73], v[84:85], v[72:73]
	v_pk_add_f32 v[68:69], v[68:69], v[74:75]
	v_pk_add_f32 v[70:71], v[70:71], v[80:81]
	v_pk_add_f32 v[74:75], v[76:77], v[82:83]
	v_pk_add_f32 v[68:69], v[72:73], v[68:69]
	v_pk_add_f32 v[70:71], v[70:71], v[74:75]
	s_nop 0
	v_pk_add_f32 v[68:69], v[68:69], v[70:71]
	v_mad_i64_i32 v[70:71], s[2:3], v66, s5, v[0:1]
	v_add_f32_e32 v68, v68, v69
	v_fmamk_f32 v68, v68, 0x3aaaaaab, v67
	v_rsq_f32_e32 v68, v68
	s_nop 0
	v_pk_mul_f32 v[62:63], v[62:63], v[68:69] op_sel_hi:[1,0]
	v_pk_mul_f32 v[64:65], v[64:65], v[68:69] op_sel_hi:[1,0]
	v_pk_mul_f32 v[58:59], v[58:59], v[68:69] op_sel_hi:[1,0]
	v_pk_mul_f32 v[60:61], v[60:61], v[68:69] op_sel_hi:[1,0]
	v_pk_mul_f32 v[54:55], v[54:55], v[68:69] op_sel_hi:[1,0]
	v_mul_f32_e32 v69, 0x3dd2d3e8, v62
	v_mul_f32_e32 v72, 0x3dd2d3e8, v63
	v_mul_f32_e32 v73, 0x3dd2d3e8, v64
	v_mul_f32_e32 v74, 0x3dd2d3e8, v65
	v_mul_f32_e32 v75, 0x3dd2d3e8, v58
	v_fma_f32 v69, -v62, v69, s4
	v_fma_f32 v72, -v63, v72, s4
	v_fma_f32 v73, -v64, v73, s4
	v_fma_f32 v74, -v65, v74, s4
	v_fma_f32 v75, -v58, v75, s4
	v_mul_f32_e32 v69, v62, v69
	v_mul_f32_e32 v72, v63, v72
	v_mul_f32_e32 v73, v64, v73
	v_mul_f32_e32 v74, v65, v74
	v_mul_f32_e32 v75, v58, v75
	v_exp_f32_e32 v69, v69
	v_exp_f32_e32 v72, v72
	v_exp_f32_e32 v73, v73
	v_exp_f32_e32 v74, v74
	v_exp_f32_e32 v75, v75
	v_add_f32_e32 v69, 1.0, v69
	v_add_f32_e32 v81, 1.0, v72
	v_add_f32_e32 v82, 1.0, v73
	v_add_f32_e32 v83, 1.0, v74
	v_add_f32_e32 v84, 1.0, v75
	v_rcp_f32_e32 v72, v69
	v_rcp_f32_e32 v73, v81
	v_rcp_f32_e32 v74, v82
	v_rcp_f32_e32 v75, v83
	v_mul_f32_e32 v76, 0x3dd2d3e8, v59
	v_mul_f32_e32 v77, 0x3dd2d3e8, v60
	v_fma_f32 v76, -v59, v76, s4
	v_fma_f32 v77, -v60, v77, s4
	v_mul_f32_e32 v76, v59, v76
	v_mul_f32_e32 v78, 0x3dd2d3e8, v61
	v_mul_f32_e32 v77, v60, v77
	v_exp_f32_e32 v76, v76
	v_pk_mul_f32 v[62:63], v[62:63], v[72:73]
	v_pk_mul_f32 v[64:65], v[64:65], v[74:75]
	v_mul_f32_e32 v79, 0x3dd2d3e8, v54
	v_fma_f32 v78, -v61, v78, s4
	v_exp_f32_e32 v77, v77
	v_cvt_pk_bf16_f32 v62, v62, v63
	v_cvt_pk_bf16_f32 v63, v64, v65
	v_pk_mul_f32 v[56:57], v[56:57], v[68:69] op_sel_hi:[1,0]
	v_fma_f32 v79, -v54, v79, s4
	v_mul_f32_e32 v78, v61, v78
	global_store_dwordx2 v[70:71], v[62:63], off
	v_mul_f32_e32 v63, 0x3dd2d3e8, v56
	v_mul_f32_e32 v80, 0x3dd2d3e8, v55
	v_mul_f32_e32 v79, v54, v79
	v_exp_f32_e32 v78, v78
	v_fma_f32 v63, -v56, v63, s4
	v_fma_f32 v80, -v55, v80, s4
	v_exp_f32_e32 v79, v79
	v_add_f32_e32 v85, 1.0, v76
	v_mul_f32_e32 v63, v56, v63
	v_mul_f32_e32 v80, v55, v80
	v_add_f32_e32 v86, 1.0, v77
	v_rcp_f32_e32 v76, v84
	v_rcp_f32_e32 v77, v85
	v_exp_f32_e32 v64, v63
	v_mul_f32_e32 v63, 0x3dd2d3e8, v57
	v_exp_f32_e32 v80, v80
	v_fma_f32 v63, -v57, v63, s4
	v_add_f32_e32 v87, 1.0, v78
	v_mul_f32_e32 v63, v57, v63
	v_add_f32_e32 v88, 1.0, v79
	v_rcp_f32_e32 v78, v86
	v_rcp_f32_e32 v79, v87
	v_exp_f32_e32 v65, v63
	v_pk_mul_f32 v[58:59], v[58:59], v[76:77]
	v_pk_mul_f32 v[50:51], v[50:51], v[68:69] op_sel_hi:[1,0]
	v_cvt_pk_bf16_f32 v58, v58, v59
	v_add_f32_e32 v59, 1.0, v80
	v_rcp_f32_e32 v63, v59
	v_add_f32_e32 v59, 1.0, v64
	v_pk_mul_f32 v[60:61], v[60:61], v[78:79]
	v_rcp_f32_e32 v64, v59
	v_add_f32_e32 v59, 1.0, v65
	v_rcp_f32_e32 v65, v59
	v_cvt_pk_bf16_f32 v59, v60, v61
	global_store_dwordx2 v[70:71], v[58:59], off offset:32
	v_mul_f32_e32 v58, 0x3dd2d3e8, v50
	v_fma_f32 v58, -v50, v58, s4
	v_mul_f32_e32 v59, 0x3dd2d3e8, v51
	v_rcp_f32_e32 v62, v88
	v_mul_f32_e32 v58, v50, v58
	v_fma_f32 v59, -v51, v59, s4
	v_exp_f32_e32 v58, v58
	v_mul_f32_e32 v59, v51, v59
	v_exp_f32_e32 v59, v59
	v_pk_mul_f32 v[54:55], v[54:55], v[62:63]
	v_pk_mul_f32 v[52:53], v[52:53], v[68:69] op_sel_hi:[1,0]
	v_cvt_pk_bf16_f32 v54, v54, v55
	v_add_f32_e32 v55, 1.0, v58
	v_rcp_f32_e32 v58, v55
	v_add_f32_e32 v55, 1.0, v59
	v_mul_f32_e32 v59, 0x3dd2d3e8, v52
	v_fma_f32 v59, -v52, v59, s4
	v_mul_f32_e32 v59, v52, v59
	v_exp_f32_e32 v60, v59
	v_mul_f32_e32 v59, 0x3dd2d3e8, v53
	v_fma_f32 v59, -v53, v59, s4
	v_mul_f32_e32 v59, v53, v59
	v_exp_f32_e32 v61, v59
	v_rcp_f32_e32 v59, v55
	v_add_f32_e32 v55, 1.0, v60
	v_rcp_f32_e32 v60, v55
	v_add_f32_e32 v55, 1.0, v61
	v_rcp_f32_e32 v61, v55
	v_pk_mul_f32 v[50:51], v[50:51], v[58:59]
	v_or_b32_e32 v68, 16, v66
	v_pk_mul_f32 v[56:57], v[56:57], v[64:65]
	v_pk_mul_f32 v[52:53], v[52:53], v[60:61]
	v_cvt_pk_bf16_f32 v50, v50, v51
	v_cvt_pk_bf16_f32 v51, v52, v53
	v_ashrrev_i32_e32 v69, 31, v68
	v_cvt_pk_bf16_f32 v55, v56, v57
	global_store_dwordx2 v[70:71], v[50:51], off offset:96
	v_lshlrev_b64 v[50:51], 6, v[68:69]
	global_store_dwordx2 v[70:71], v[54:55], off offset:64
	v_lshl_add_u64 v[70:71], s[0:1], 0, v[50:51]
	global_load_dwordx4 v[50:53], v[70:71], off
	global_load_dwordx4 v[54:57], v[70:71], off offset:32
	global_load_dwordx4 v[58:61], v[70:71], off offset:16
	global_load_dwordx4 v[62:65], v[70:71], off offset:48
	s_waitcnt vmcnt(3)
	v_mov_b32_e32 v70, v50
	s_waitcnt vmcnt(2)
	v_mov_b32_e32 v71, v54
	v_mov_b32_e32 v54, v51
	v_mov_b32_e32 v50, v52
	v_mov_b32_e32 v51, v56
	v_mov_b32_e32 v56, v53
	s_waitcnt vmcnt(1)
	v_mov_b32_e32 v52, v58
	s_waitcnt vmcnt(0)
	v_mov_b32_e32 v53, v62
	v_mov_b32_e32 v62, v59
	v_mov_b32_e32 v58, v60
	v_mov_b32_e32 v59, v64
	v_mov_b32_e32 v64, v61
	v_pk_add_f32 v[54:55], v[70:71], v[54:55]
	v_pk_add_f32 v[50:51], v[50:51], v[56:57]
	v_pk_add_f32 v[52:53], v[52:53], v[62:63]
	v_pk_add_f32 v[56:57], v[58:59], v[64:65]
	v_pk_add_f32 v[50:51], v[54:55], v[50:51]
	v_pk_add_f32 v[52:53], v[52:53], v[56:57]
	v_mad_i64_i32 v[56:57], s[2:3], v68, s5, v[0:1]
	v_pk_add_f32 v[50:51], v[50:51], v[52:53]
	s_nop 0
	v_add_f32_e32 v50, v50, v51
	v_fmamk_f32 v50, v50, 0x3aaaaaab, v67
	v_rsq_f32_e32 v50, v50
	s_nop 0
	v_pk_mul_f32 v[46:47], v[46:47], v[50:51] op_sel_hi:[1,0]
	v_pk_mul_f32 v[48:49], v[48:49], v[50:51] op_sel_hi:[1,0]
	v_mul_f32_e32 v51, 0x3dd2d3e8, v46
	v_mul_f32_e32 v52, 0x3dd2d3e8, v47
	v_fma_f32 v51, -v46, v51, s4
	v_fma_f32 v52, -v47, v52, s4
	v_mul_f32_e32 v51, v46, v51
	v_mul_f32_e32 v52, v47, v52
	v_exp_f32_e32 v51, v51
	v_exp_f32_e32 v52, v52
	v_mul_f32_e32 v53, 0x3dd2d3e8, v48
	v_fma_f32 v53, -v48, v53, s4
	v_mul_f32_e32 v53, v48, v53
	v_add_f32_e32 v51, 1.0, v51
	v_add_f32_e32 v54, 1.0, v52
	v_rcp_f32_e32 v52, v51
	v_exp_f32_e32 v51, v53
	v_mul_f32_e32 v53, 0x3dd2d3e8, v49
	v_fma_f32 v53, -v49, v53, s4
	v_mul_f32_e32 v53, v49, v53
	v_exp_f32_e32 v55, v53
	v_add_f32_e32 v51, 1.0, v51
	v_rcp_f32_e32 v53, v54
	v_rcp_f32_e32 v54, v51
	v_add_f32_e32 v51, 1.0, v55
	v_pk_mul_f32 v[42:43], v[42:43], v[50:51] op_sel_hi:[1,0]
	v_rcp_f32_e32 v55, v51
	v_mul_f32_e32 v51, 0x3dd2d3e8, v42
	v_fma_f32 v51, -v42, v51, s4
	v_pk_mul_f32 v[46:47], v[46:47], v[52:53]
	v_mul_f32_e32 v51, v42, v51
	v_mul_f32_e32 v52, 0x3dd2d3e8, v43
	v_exp_f32_e32 v51, v51
	v_fma_f32 v52, -v43, v52, s4
	v_mul_f32_e32 v52, v43, v52
	v_exp_f32_e32 v53, v52
	v_pk_mul_f32 v[44:45], v[44:45], v[50:51] op_sel_hi:[1,0]
	v_cvt_pk_bf16_f32 v46, v46, v47
	v_add_f32_e32 v47, 1.0, v51
	v_mul_f32_e32 v51, 0x3dd2d3e8, v44
	v_rcp_f32_e32 v52, v47
	v_add_f32_e32 v47, 1.0, v53
	v_fma_f32 v51, -v44, v51, s4
	v_mul_f32_e32 v53, 0x3dd2d3e8, v45
	v_mul_f32_e32 v51, v44, v51
	v_fma_f32 v53, -v45, v53, s4
	v_exp_f32_e32 v51, v51
	v_mul_f32_e32 v53, v45, v53
	v_pk_mul_f32 v[48:49], v[48:49], v[54:55]
	v_exp_f32_e32 v55, v53
	v_rcp_f32_e32 v53, v47
	v_add_f32_e32 v47, 1.0, v51
	v_rcp_f32_e32 v54, v47
	v_add_f32_e32 v47, 1.0, v55
	v_rcp_f32_e32 v55, v47
	v_cvt_pk_bf16_f32 v47, v48, v49
	v_pk_mul_f32 v[38:39], v[38:39], v[50:51] op_sel_hi:[1,0]
	global_store_dwordx2 v[56:57], v[46:47], off
	v_mul_f32_e32 v46, 0x3dd2d3e8, v38
	v_fma_f32 v46, -v38, v46, s4
	v_mul_f32_e32 v47, 0x3dd2d3e8, v39
	v_mul_f32_e32 v46, v38, v46
	v_fma_f32 v47, -v39, v47, s4
	v_exp_f32_e32 v46, v46
	v_mul_f32_e32 v47, v39, v47
	v_exp_f32_e32 v47, v47
	v_pk_mul_f32 v[42:43], v[42:43], v[52:53]
	v_pk_mul_f32 v[40:41], v[40:41], v[50:51] op_sel_hi:[1,0]
	v_cvt_pk_bf16_f32 v42, v42, v43
	v_add_f32_e32 v43, 1.0, v46
	v_rcp_f32_e32 v46, v43
	v_add_f32_e32 v43, 1.0, v47
	v_mul_f32_e32 v47, 0x3dd2d3e8, v40
	v_fma_f32 v47, -v40, v47, s4
	v_mul_f32_e32 v47, v40, v47
	v_exp_f32_e32 v48, v47
	v_mul_f32_e32 v47, 0x3dd2d3e8, v41
	v_fma_f32 v47, -v41, v47, s4
	v_mul_f32_e32 v47, v41, v47
	v_exp_f32_e32 v49, v47
	v_rcp_f32_e32 v47, v43
	v_add_f32_e32 v43, 1.0, v48
	v_pk_mul_f32 v[44:45], v[44:45], v[54:55]
	v_rcp_f32_e32 v48, v43
	v_add_f32_e32 v43, 1.0, v49
	v_rcp_f32_e32 v49, v43
	v_cvt_pk_bf16_f32 v43, v44, v45
	v_pk_mul_f32 v[34:35], v[34:35], v[50:51] op_sel_hi:[1,0]
	global_store_dwordx2 v[56:57], v[42:43], off offset:32
	v_mul_f32_e32 v42, 0x3dd2d3e8, v34
	v_fma_f32 v42, -v34, v42, s4
	v_mul_f32_e32 v43, 0x3dd2d3e8, v35
	v_mul_f32_e32 v42, v34, v42
	v_fma_f32 v43, -v35, v43, s4
	v_exp_f32_e32 v42, v42
	v_mul_f32_e32 v43, v35, v43
	v_exp_f32_e32 v43, v43
	v_pk_mul_f32 v[38:39], v[38:39], v[46:47]
	v_pk_mul_f32 v[36:37], v[36:37], v[50:51] op_sel_hi:[1,0]
	v_cvt_pk_bf16_f32 v38, v38, v39
	v_add_f32_e32 v39, 1.0, v42
	v_rcp_f32_e32 v42, v39
	v_add_f32_e32 v39, 1.0, v43
	v_mul_f32_e32 v43, 0x3dd2d3e8, v36
	v_fma_f32 v43, -v36, v43, s4
	v_mul_f32_e32 v43, v36, v43
	v_exp_f32_e32 v44, v43
	v_mul_f32_e32 v43, 0x3dd2d3e8, v37
	v_fma_f32 v43, -v37, v43, s4
	v_mul_f32_e32 v43, v37, v43
	v_exp_f32_e32 v45, v43
	v_rcp_f32_e32 v43, v39
	v_add_f32_e32 v39, 1.0, v44
	v_rcp_f32_e32 v44, v39
	v_add_f32_e32 v39, 1.0, v45
	v_rcp_f32_e32 v45, v39
	v_pk_mul_f32 v[34:35], v[34:35], v[42:43]
	v_or_b32_e32 v50, 32, v66
	v_pk_mul_f32 v[40:41], v[40:41], v[48:49]
	v_pk_mul_f32 v[36:37], v[36:37], v[44:45]
	v_cvt_pk_bf16_f32 v34, v34, v35
	v_cvt_pk_bf16_f32 v35, v36, v37
	v_ashrrev_i32_e32 v51, 31, v50
	v_cvt_pk_bf16_f32 v39, v40, v41
	global_store_dwordx2 v[56:57], v[34:35], off offset:96
	v_lshlrev_b64 v[34:35], 6, v[50:51]
	global_store_dwordx2 v[56:57], v[38:39], off offset:64
	v_lshl_add_u64 v[52:53], s[0:1], 0, v[34:35]
	global_load_dwordx4 v[34:37], v[52:53], off
	global_load_dwordx4 v[38:41], v[52:53], off offset:32
	global_load_dwordx4 v[42:45], v[52:53], off offset:16
	global_load_dwordx4 v[46:49], v[52:53], off offset:48
	s_waitcnt vmcnt(3)
	v_mov_b32_e32 v52, v34
	s_waitcnt vmcnt(2)
	v_mov_b32_e32 v53, v38
	v_mov_b32_e32 v38, v35
	v_pk_add_f32 v[34:35], v[52:53], v[38:39]
	v_mov_b32_e32 v38, v36
	v_mov_b32_e32 v39, v40
	v_mov_b32_e32 v40, v37
	v_pk_add_f32 v[36:37], v[38:39], v[40:41]
	s_waitcnt vmcnt(1)
	v_mov_b32_e32 v38, v44
	v_pk_add_f32 v[34:35], v[34:35], v[36:37]
	v_mov_b32_e32 v36, v42
	s_waitcnt vmcnt(0)
	v_mov_b32_e32 v37, v46
	v_mov_b32_e32 v46, v43
	v_mov_b32_e32 v39, v48
	v_mov_b32_e32 v48, v45
	v_pk_add_f32 v[36:37], v[36:37], v[46:47]
	v_pk_add_f32 v[38:39], v[38:39], v[48:49]
	v_mad_i64_i32 v[40:41], s[2:3], v50, s5, v[0:1]
	v_pk_add_f32 v[36:37], v[36:37], v[38:39]
	s_nop 0
	v_pk_add_f32 v[34:35], v[34:35], v[36:37]
	s_nop 0
	v_add_f32_e32 v34, v34, v35
	v_fmamk_f32 v34, v34, 0x3aaaaaab, v67
	v_rsq_f32_e32 v34, v34
	s_nop 0
	v_pk_mul_f32 v[30:31], v[30:31], v[34:35] op_sel_hi:[1,0]
	s_nop 0
	v_mul_f32_e32 v35, 0x3dd2d3e8, v30
	v_fma_f32 v35, -v30, v35, s4
	v_mul_f32_e32 v36, 0x3dd2d3e8, v31
	v_mul_f32_e32 v35, v30, v35
	v_fma_f32 v36, -v31, v36, s4
	v_exp_f32_e32 v35, v35
	v_mul_f32_e32 v36, v31, v36
	v_exp_f32_e32 v37, v36
	v_add_f32_e32 v35, 1.0, v35
	v_rcp_f32_e32 v36, v35
	v_add_f32_e32 v35, 1.0, v37
	v_pk_mul_f32 v[32:33], v[32:33], v[34:35] op_sel_hi:[1,0]
	s_nop 0
	v_mul_f32_e32 v37, 0x3dd2d3e8, v32
	v_fma_f32 v37, -v32, v37, s4
	v_mul_f32_e32 v37, v32, v37
	v_exp_f32_e32 v38, v37
	v_mul_f32_e32 v37, 0x3dd2d3e8, v33
	v_fma_f32 v37, -v33, v37, s4
	v_mul_f32_e32 v37, v33, v37
	v_exp_f32_e32 v39, v37
	v_rcp_f32_e32 v37, v35
	v_add_f32_e32 v35, 1.0, v38
	v_rcp_f32_e32 v38, v35
	v_add_f32_e32 v35, 1.0, v39
	v_pk_mul_f32 v[26:27], v[26:27], v[34:35] op_sel_hi:[1,0]
	v_rcp_f32_e32 v39, v35
	v_mul_f32_e32 v35, 0x3dd2d3e8, v26
	v_fma_f32 v35, -v26, v35, s4
	v_pk_mul_f32 v[30:31], v[30:31], v[36:37]
	v_mul_f32_e32 v35, v26, v35
	v_mul_f32_e32 v36, 0x3dd2d3e8, v27
	v_exp_f32_e32 v35, v35
	v_fma_f32 v36, -v27, v36, s4
	v_mul_f32_e32 v36, v27, v36
	v_exp_f32_e32 v37, v36
	v_pk_mul_f32 v[28:29], v[28:29], v[34:35] op_sel_hi:[1,0]
	v_cvt_pk_bf16_f32 v30, v30, v31
	v_add_f32_e32 v31, 1.0, v35
	v_mul_f32_e32 v35, 0x3dd2d3e8, v28
	v_rcp_f32_e32 v36, v31
	v_add_f32_e32 v31, 1.0, v37
	v_fma_f32 v35, -v28, v35, s4
	v_mul_f32_e32 v37, 0x3dd2d3e8, v29
	v_mul_f32_e32 v35, v28, v35
	v_fma_f32 v37, -v29, v37, s4
	v_exp_f32_e32 v35, v35
	v_mul_f32_e32 v37, v29, v37
	v_pk_mul_f32 v[32:33], v[32:33], v[38:39]
	v_exp_f32_e32 v39, v37
	v_rcp_f32_e32 v37, v31
	v_add_f32_e32 v31, 1.0, v35
	v_rcp_f32_e32 v38, v31
	v_add_f32_e32 v31, 1.0, v39
	v_rcp_f32_e32 v39, v31
	v_cvt_pk_bf16_f32 v31, v32, v33
	v_pk_mul_f32 v[22:23], v[22:23], v[34:35] op_sel_hi:[1,0]
	global_store_dwordx2 v[40:41], v[30:31], off
	v_mul_f32_e32 v30, 0x3dd2d3e8, v22
	v_fma_f32 v30, -v22, v30, s4
	v_mul_f32_e32 v31, 0x3dd2d3e8, v23
	v_mul_f32_e32 v30, v22, v30
	v_fma_f32 v31, -v23, v31, s4
	v_exp_f32_e32 v30, v30
	v_mul_f32_e32 v31, v23, v31
	v_exp_f32_e32 v31, v31
	v_pk_mul_f32 v[26:27], v[26:27], v[36:37]
	v_pk_mul_f32 v[24:25], v[24:25], v[34:35] op_sel_hi:[1,0]
	v_cvt_pk_bf16_f32 v26, v26, v27
	v_add_f32_e32 v27, 1.0, v30
	v_rcp_f32_e32 v30, v27
	v_add_f32_e32 v27, 1.0, v31
	v_mul_f32_e32 v31, 0x3dd2d3e8, v24
	v_fma_f32 v31, -v24, v31, s4
	v_mul_f32_e32 v31, v24, v31
	v_exp_f32_e32 v32, v31
	v_mul_f32_e32 v31, 0x3dd2d3e8, v25
	v_fma_f32 v31, -v25, v31, s4
	v_mul_f32_e32 v31, v25, v31
	v_exp_f32_e32 v33, v31
	v_rcp_f32_e32 v31, v27
	v_add_f32_e32 v27, 1.0, v32
	v_pk_mul_f32 v[28:29], v[28:29], v[38:39]
	v_rcp_f32_e32 v32, v27
	v_add_f32_e32 v27, 1.0, v33
	v_rcp_f32_e32 v33, v27
	v_cvt_pk_bf16_f32 v27, v28, v29
	v_pk_mul_f32 v[18:19], v[18:19], v[34:35] op_sel_hi:[1,0]
	global_store_dwordx2 v[40:41], v[26:27], off offset:32
	v_mul_f32_e32 v26, 0x3dd2d3e8, v18
	v_fma_f32 v26, -v18, v26, s4
	v_mul_f32_e32 v27, 0x3dd2d3e8, v19
	v_mul_f32_e32 v26, v18, v26
	v_fma_f32 v27, -v19, v27, s4
	v_exp_f32_e32 v26, v26
	v_mul_f32_e32 v27, v19, v27
	v_exp_f32_e32 v27, v27
	v_pk_mul_f32 v[22:23], v[22:23], v[30:31]
	v_pk_mul_f32 v[20:21], v[20:21], v[34:35] op_sel_hi:[1,0]
	v_cvt_pk_bf16_f32 v22, v22, v23
	v_add_f32_e32 v23, 1.0, v26
	v_rcp_f32_e32 v26, v23
	v_add_f32_e32 v23, 1.0, v27
	v_mul_f32_e32 v27, 0x3dd2d3e8, v20
	v_fma_f32 v27, -v20, v27, s4
	v_mul_f32_e32 v27, v20, v27
	v_exp_f32_e32 v28, v27
	v_mul_f32_e32 v27, 0x3dd2d3e8, v21
	v_fma_f32 v27, -v21, v27, s4
	v_mul_f32_e32 v27, v21, v27
	v_exp_f32_e32 v29, v27
	v_rcp_f32_e32 v27, v23
	v_add_f32_e32 v23, 1.0, v28
	v_rcp_f32_e32 v28, v23
	v_add_f32_e32 v23, 1.0, v29
	v_rcp_f32_e32 v29, v23
	v_pk_mul_f32 v[18:19], v[18:19], v[26:27]
	v_or_b32_e32 v34, 48, v66
	v_pk_mul_f32 v[24:25], v[24:25], v[32:33]
	v_pk_mul_f32 v[20:21], v[20:21], v[28:29]
	v_cvt_pk_bf16_f32 v18, v18, v19
	v_cvt_pk_bf16_f32 v19, v20, v21
	v_ashrrev_i32_e32 v35, 31, v34
	v_cvt_pk_bf16_f32 v23, v24, v25
	global_store_dwordx2 v[40:41], v[18:19], off offset:96
	v_lshlrev_b64 v[18:19], 6, v[34:35]
	global_store_dwordx2 v[40:41], v[22:23], off offset:64
	v_lshl_add_u64 v[36:37], s[0:1], 0, v[18:19]
	global_load_dwordx4 v[18:21], v[36:37], off
	global_load_dwordx4 v[22:25], v[36:37], off offset:32
	global_load_dwordx4 v[26:29], v[36:37], off offset:16
	global_load_dwordx4 v[30:33], v[36:37], off offset:48
	v_mad_i64_i32 v[0:1], s[0:1], v34, s5, v[0:1]
	s_waitcnt vmcnt(3)
	v_mov_b32_e32 v36, v18
	s_waitcnt vmcnt(2)
	v_mov_b32_e32 v37, v22
	v_mov_b32_e32 v22, v19
	v_pk_add_f32 v[18:19], v[36:37], v[22:23]
	v_mov_b32_e32 v22, v20
	v_mov_b32_e32 v23, v24
	v_mov_b32_e32 v24, v21
	v_pk_add_f32 v[20:21], v[22:23], v[24:25]
	s_waitcnt vmcnt(1)
	v_mov_b32_e32 v22, v28
	v_pk_add_f32 v[18:19], v[18:19], v[20:21]
	v_mov_b32_e32 v20, v26
	s_waitcnt vmcnt(0)
	v_mov_b32_e32 v21, v30
	v_mov_b32_e32 v30, v27
	v_mov_b32_e32 v23, v32
	v_mov_b32_e32 v32, v29
	v_pk_add_f32 v[20:21], v[20:21], v[30:31]
	v_pk_add_f32 v[22:23], v[22:23], v[32:33]
	s_nop 0
	v_pk_add_f32 v[20:21], v[20:21], v[22:23]
	s_nop 0
	v_pk_add_f32 v[18:19], v[18:19], v[20:21]
	s_nop 0
	v_add_f32_e32 v18, v18, v19
	v_fmac_f32_e32 v67, 0x3aaaaaab, v18
	v_rsq_f32_e32 v18, v67
	s_nop 0
	v_pk_mul_f32 v[14:15], v[14:15], v[18:19] op_sel_hi:[1,0]
	s_nop 0
	v_mul_f32_e32 v19, 0x3dd2d3e8, v14
	v_fma_f32 v19, -v14, v19, s4
	v_mul_f32_e32 v20, 0x3dd2d3e8, v15
	v_mul_f32_e32 v19, v14, v19
	v_fma_f32 v20, -v15, v20, s4
	v_exp_f32_e32 v19, v19
	v_mul_f32_e32 v20, v15, v20
	v_exp_f32_e32 v21, v20
	v_add_f32_e32 v19, 1.0, v19
	v_rcp_f32_e32 v20, v19
	v_add_f32_e32 v19, 1.0, v21
	v_pk_mul_f32 v[16:17], v[16:17], v[18:19] op_sel_hi:[1,0]
	s_nop 0
	v_mul_f32_e32 v21, 0x3dd2d3e8, v16
	v_fma_f32 v21, -v16, v21, s4
	v_mul_f32_e32 v21, v16, v21
	v_exp_f32_e32 v22, v21
	v_mul_f32_e32 v21, 0x3dd2d3e8, v17
	v_fma_f32 v21, -v17, v21, s4
	v_mul_f32_e32 v21, v17, v21
	v_exp_f32_e32 v23, v21
	v_rcp_f32_e32 v21, v19
	v_add_f32_e32 v19, 1.0, v22
	v_rcp_f32_e32 v22, v19
	v_add_f32_e32 v19, 1.0, v23
	v_pk_mul_f32 v[10:11], v[10:11], v[18:19] op_sel_hi:[1,0]
	v_rcp_f32_e32 v23, v19
	v_mul_f32_e32 v19, 0x3dd2d3e8, v10
	v_fma_f32 v19, -v10, v19, s4
	v_pk_mul_f32 v[14:15], v[14:15], v[20:21]
	v_mul_f32_e32 v19, v10, v19
	v_mul_f32_e32 v20, 0x3dd2d3e8, v11
	v_exp_f32_e32 v19, v19
	v_fma_f32 v20, -v11, v20, s4
	v_mul_f32_e32 v20, v11, v20
	v_exp_f32_e32 v21, v20
	v_pk_mul_f32 v[12:13], v[12:13], v[18:19] op_sel_hi:[1,0]
	v_cvt_pk_bf16_f32 v14, v14, v15
	v_add_f32_e32 v15, 1.0, v19
	v_mul_f32_e32 v19, 0x3dd2d3e8, v12
	v_rcp_f32_e32 v20, v15
	v_add_f32_e32 v15, 1.0, v21
	v_fma_f32 v19, -v12, v19, s4
	v_mul_f32_e32 v21, 0x3dd2d3e8, v13
	v_mul_f32_e32 v19, v12, v19
	v_fma_f32 v21, -v13, v21, s4
	v_exp_f32_e32 v19, v19
	v_mul_f32_e32 v21, v13, v21
	v_pk_mul_f32 v[16:17], v[16:17], v[22:23]
	v_exp_f32_e32 v23, v21
	v_rcp_f32_e32 v21, v15
	v_add_f32_e32 v15, 1.0, v19
	v_rcp_f32_e32 v22, v15
	v_add_f32_e32 v15, 1.0, v23
	v_rcp_f32_e32 v23, v15
	v_cvt_pk_bf16_f32 v15, v16, v17
	v_pk_mul_f32 v[6:7], v[6:7], v[18:19] op_sel_hi:[1,0]
	global_store_dwordx2 v[0:1], v[14:15], off
	v_mul_f32_e32 v14, 0x3dd2d3e8, v6
	v_fma_f32 v14, -v6, v14, s4
	v_mul_f32_e32 v15, 0x3dd2d3e8, v7
	v_mul_f32_e32 v14, v6, v14
	v_fma_f32 v15, -v7, v15, s4
	v_exp_f32_e32 v14, v14
	v_mul_f32_e32 v15, v7, v15
	v_exp_f32_e32 v15, v15
	v_pk_mul_f32 v[10:11], v[10:11], v[20:21]
	v_pk_mul_f32 v[8:9], v[8:9], v[18:19] op_sel_hi:[1,0]
	v_cvt_pk_bf16_f32 v10, v10, v11
	v_add_f32_e32 v11, 1.0, v14
	v_rcp_f32_e32 v14, v11
	v_add_f32_e32 v11, 1.0, v15
	v_mul_f32_e32 v15, 0x3dd2d3e8, v8
	v_fma_f32 v15, -v8, v15, s4
	v_mul_f32_e32 v15, v8, v15
	v_exp_f32_e32 v16, v15
	v_mul_f32_e32 v15, 0x3dd2d3e8, v9
	v_fma_f32 v15, -v9, v15, s4
	v_mul_f32_e32 v15, v9, v15
	v_exp_f32_e32 v17, v15
	v_rcp_f32_e32 v15, v11
	v_add_f32_e32 v11, 1.0, v16
	v_pk_mul_f32 v[12:13], v[12:13], v[22:23]
	v_rcp_f32_e32 v16, v11
	v_add_f32_e32 v11, 1.0, v17
	v_rcp_f32_e32 v17, v11
	v_cvt_pk_bf16_f32 v11, v12, v13
	v_pk_mul_f32 v[2:3], v[2:3], v[18:19] op_sel_hi:[1,0]
	global_store_dwordx2 v[0:1], v[10:11], off offset:32
	v_mul_f32_e32 v10, 0x3dd2d3e8, v2
	v_fma_f32 v10, -v2, v10, s4
	v_mul_f32_e32 v11, 0x3dd2d3e8, v3
	v_mul_f32_e32 v10, v2, v10
	v_fma_f32 v11, -v3, v11, s4
	v_exp_f32_e32 v10, v10
	v_mul_f32_e32 v11, v3, v11
	v_exp_f32_e32 v11, v11
	v_pk_mul_f32 v[6:7], v[6:7], v[14:15]
	v_pk_mul_f32 v[4:5], v[4:5], v[18:19] op_sel_hi:[1,0]
	v_cvt_pk_bf16_f32 v6, v6, v7
	v_add_f32_e32 v7, 1.0, v10
	v_rcp_f32_e32 v10, v7
	v_add_f32_e32 v7, 1.0, v11
	v_mul_f32_e32 v11, 0x3dd2d3e8, v4
	v_fma_f32 v11, -v4, v11, s4
	v_mul_f32_e32 v11, v4, v11
	v_exp_f32_e32 v12, v11
	v_mul_f32_e32 v11, 0x3dd2d3e8, v5
	v_fma_f32 v11, -v5, v11, s4
	v_mul_f32_e32 v11, v5, v11
	v_exp_f32_e32 v13, v11
	v_rcp_f32_e32 v11, v7
	v_add_f32_e32 v7, 1.0, v12
	v_rcp_f32_e32 v12, v7
	v_add_f32_e32 v7, 1.0, v13
	v_rcp_f32_e32 v13, v7
	v_pk_mul_f32 v[8:9], v[8:9], v[16:17]
	v_pk_mul_f32 v[2:3], v[2:3], v[10:11]
	v_cvt_pk_bf16_f32 v7, v8, v9
	v_pk_mul_f32 v[4:5], v[4:5], v[12:13]
	v_cvt_pk_bf16_f32 v2, v2, v3
	v_cvt_pk_bf16_f32 v3, v4, v5
	global_store_dwordx2 v[0:1], v[6:7], off offset:64
	global_store_dwordx2 v[0:1], v[2:3], off offset:96
	s_endpgm
	.p2align	8

.LBB4_4:
	v_bfe_i32 v2, v0, 6, 1
	v_mov_b32_e32 v49, 0
	v_and_b32_e32 v123, 15, v0
	v_lshrrev_b32_e32 v124, 7, v0
	v_bfe_u32 v125, v0, 4, 2
	v_and_b32_e32 v126, 48, v2
	s_load_dwordx2 s[16:17], s[0:1], 0x20
	v_lshl_or_b32 v132, v125, 2, v126
	v_add_u32_e32 v132, s9, v132
	v_or_b32_e32 v134, s8, v123
	v_lshl_add_u32 v134, v124, 6, v134
	v_ashrrev_i32_e32 v133, 31, v132
	v_lshlrev_b64 v[132:133], 2, v[132:133]
	s_movk_i32 s18, 0xc00
	s_waitcnt lgkmcnt(0)
	v_lshl_add_u64 v[132:133], s[16:17], 0, v[132:133]
	v_mad_i64_i32 v[136:137], s[12:13], v134, s18, v[132:133]
	v_or_b32_e32 v135, 16, v134
	global_load_dwordx4 v[140:143], v[136:137], off
	global_load_dwordx4 v[144:147], v[136:137], off offset:64
	global_load_dwordx4 v[148:151], v[136:137], off offset:128
	v_mad_i64_i32 v[136:137], s[12:13], v135, s18, v[132:133]
	v_or_b32_e32 v135, 32, v134
	global_load_dwordx4 v[152:155], v[136:137], off
	global_load_dwordx4 v[156:159], v[136:137], off offset:64
	global_load_dwordx4 v[160:163], v[136:137], off offset:128
	v_mad_i64_i32 v[136:137], s[12:13], v135, s18, v[132:133]
	v_or_b32_e32 v135, 48, v134
	global_load_dwordx4 v[164:167], v[136:137], off
	global_load_dwordx4 v[168:171], v[136:137], off offset:64
	global_load_dwordx4 v[172:175], v[136:137], off offset:128
	v_mad_i64_i32 v[136:137], s[12:13], v135, s18, v[132:133]
	s_nop 0
	global_load_dwordx4 v[176:179], v[136:137], off
	global_load_dwordx4 v[180:183], v[136:137], off offset:64
	global_load_dwordx4 v[184:187], v[136:137], off offset:128
	s_cmp_lt_i32 s10, 64
	v_mov_b32_e32 v48, v49
	v_mov_b32_e32 v47, v49
	v_mov_b32_e32 v46, v49
	v_mov_b32_e32 v37, v49
	v_mov_b32_e32 v36, v49
	v_mov_b32_e32 v35, v49
	v_mov_b32_e32 v34, v49
	v_mov_b32_e32 v25, v49
	v_mov_b32_e32 v24, v49
	v_mov_b32_e32 v23, v49
	v_mov_b32_e32 v22, v49
	v_mov_b32_e32 v13, v49
	v_mov_b32_e32 v12, v49
	v_mov_b32_e32 v11, v49
	v_mov_b32_e32 v10, v49
	v_mov_b32_e32 v45, v49
	v_mov_b32_e32 v44, v49
	v_mov_b32_e32 v43, v49
	v_mov_b32_e32 v42, v49
	v_mov_b32_e32 v33, v49
	v_mov_b32_e32 v32, v49
	v_mov_b32_e32 v31, v49
	v_mov_b32_e32 v30, v49
	v_mov_b32_e32 v21, v49
	v_mov_b32_e32 v20, v49
	v_mov_b32_e32 v19, v49
	v_mov_b32_e32 v18, v49
	v_mov_b32_e32 v9, v49
	v_mov_b32_e32 v8, v49
	v_mov_b32_e32 v7, v49
	v_mov_b32_e32 v6, v49
	v_mov_b32_e32 v41, v49
	v_mov_b32_e32 v40, v49
	v_mov_b32_e32 v39, v49
	v_mov_b32_e32 v38, v49
	v_mov_b32_e32 v29, v49
	v_mov_b32_e32 v28, v49
	v_mov_b32_e32 v27, v49
	v_mov_b32_e32 v26, v49
	v_mov_b32_e32 v17, v49
	v_mov_b32_e32 v16, v49
	v_mov_b32_e32 v15, v49
	v_mov_b32_e32 v14, v49
	v_mov_b32_e32 v5, v49
	v_mov_b32_e32 v4, v49
	v_mov_b32_e32 v3, v49
	v_mov_b32_e32 v2, v49
	s_barrier
	s_cbranch_scc1 .LBB4_15
	v_lshrrev_b32_e32 v2, 1, v0
	v_bfe_u32 v0, v0, 1, 3
	v_bitop3_b32 v0, v125, v0, 4 bitop3:0x36
	v_lshlrev_b32_e32 v130, 4, v0
	v_or_b32_e32 v0, v126, v123
	v_bitop3_b32 v2, v125, v2, 7 bitop3:0x78
	v_lshlrev_b32_e32 v131, 7, v0
	v_lshlrev_b32_e32 v127, 4, v2
	v_lshlrev_b32_e32 v128, 13, v124
	v_lshlrev_b32_e32 v129, 7, v123
	v_add_u32_e32 v0, 0, v131
	v_add_u32_e32 v46, v0, v130
	v_add_u32_e32 v47, v0, v127
	v_add3_u32 v0, 0, v128, v129
	v_add_u32_e32 v48, v0, v130
	v_add_u32_e32 v49, v0, v127
	v_mad_u64_u32 v[0:1], s[4:5], v1, s10, 0
	v_mov_b32_e32 v2, v1
	v_mad_u64_u32 v[2:3], s[4:5], v62, s10, v[2:3]
	v_mad_u64_u32 v[110:111], s[4:5], v50, s10, 0
	v_mov_b32_e32 v1, v2
	v_mov_b32_e32 v2, v111
	v_mad_u64_u32 v[2:3], s[4:5], v61, s10, v[2:3]
	v_mad_u64_u32 v[112:113], s[4:5], v51, s10, 0
	v_mov_b32_e32 v111, v2
	v_mov_b32_e32 v2, v113
	v_mad_u64_u32 v[2:3], s[4:5], v60, s10, v[2:3]
	v_mad_u64_u32 v[114:115], s[4:5], v52, s10, 0
	v_mov_b32_e32 v113, v2
	v_mov_b32_e32 v2, v115
	v_mad_u64_u32 v[2:3], s[4:5], v59, s10, v[2:3]
	v_mad_u64_u32 v[116:117], s[4:5], v53, s10, 0
	v_mov_b32_e32 v115, v2
	v_mov_b32_e32 v2, v117
	v_mad_u64_u32 v[2:3], s[4:5], v58, s10, v[2:3]
	v_mad_u64_u32 v[118:119], s[4:5], v54, s10, 0
	v_mov_b32_e32 v117, v2
	v_mov_b32_e32 v2, v119
	v_mad_u64_u32 v[2:3], s[4:5], v57, s10, v[2:3]
	v_mad_u64_u32 v[120:121], s[4:5], v55, s10, 0
	v_mov_b32_e32 v119, v2
	v_mov_b32_e32 v2, v121
	v_mad_u64_u32 v[2:3], s[4:5], v56, s10, v[2:3]
	ds_read_b128 v[94:97], v46 offset:18432
	ds_read_b128 v[82:85], v46 offset:16384
	ds_read_b128 v[98:101], v47 offset:20480
	ds_read_b128 v[90:93], v47 offset:18432
	ds_read_b128 v[102:105], v46 offset:20480
	ds_read_b128 v[86:89], v47 offset:16384
	ds_read_b128 v[70:73], v48 offset:6144
	ds_read_b128 v[66:69], v48 offset:4096
	ds_read_b128 v[54:57], v48 offset:2048
	ds_read_b128 v[50:53], v48
	ds_read_b128 v[78:81], v49 offset:6144
	ds_read_b128 v[74:77], v49 offset:4096
	ds_read_b128 v[62:65], v49 offset:2048
	ds_read_b128 v[58:61], v49
	s_ashr_i32 s2, s10, 31
	s_lshr_b32 s2, s2, 26
	s_add_i32 s2, s10, s2
	s_mov_b32 s3, 0
	v_mov_b32_e32 v121, v2
	v_mov_b32_e32 v2, 0
	s_ashr_i32 s6, s2, 6
	s_movk_i32 s2, 0x80
	s_mov_b32 s7, s3
	v_mov_b32_e32 v3, v2
	v_mov_b32_e32 v4, v2
	v_mov_b32_e32 v5, v2
	v_mov_b32_e32 v14, v2
	v_mov_b32_e32 v15, v2
	v_mov_b32_e32 v16, v2
	v_mov_b32_e32 v17, v2
	v_mov_b32_e32 v26, v2
	v_mov_b32_e32 v27, v2
	v_mov_b32_e32 v28, v2
	v_mov_b32_e32 v29, v2
	v_mov_b32_e32 v38, v2
	v_mov_b32_e32 v39, v2
	v_mov_b32_e32 v40, v2
	v_mov_b32_e32 v41, v2
	v_mov_b32_e32 v6, v2
	v_mov_b32_e32 v7, v2
	v_mov_b32_e32 v8, v2
	v_mov_b32_e32 v9, v2
	v_mov_b32_e32 v18, v2
	v_mov_b32_e32 v19, v2
	v_mov_b32_e32 v20, v2
	v_mov_b32_e32 v21, v2
	v_mov_b32_e32 v30, v2
	v_mov_b32_e32 v31, v2
	v_mov_b32_e32 v32, v2
	v_mov_b32_e32 v33, v2
	v_mov_b32_e32 v42, v2
	v_mov_b32_e32 v43, v2
	v_mov_b32_e32 v44, v2
	v_mov_b32_e32 v45, v2
	v_mov_b32_e32 v10, v2
	v_mov_b32_e32 v11, v2
	v_mov_b32_e32 v12, v2
	v_mov_b32_e32 v13, v2
	v_mov_b32_e32 v22, v2
	v_mov_b32_e32 v23, v2
	v_mov_b32_e32 v24, v2
	v_mov_b32_e32 v25, v2
	v_mov_b32_e32 v34, v2
	v_mov_b32_e32 v35, v2
	v_mov_b32_e32 v36, v2
	v_mov_b32_e32 v37, v2
	v_mov_b32_e32 v46, v2
	v_mov_b32_e32 v47, v2
	v_mov_b32_e32 v48, v2
	v_mov_b32_e32 v49, v2
	s_branch .LBB4_8

.LBB4_15:
	s_load_dwordx2 s[2:3], s[0:1], 0x38
	v_lshl_or_b32 v0, v125, 2, v126
	v_add_u32_e32 v0, s9, v0
	v_or_b32_e32 v1, s8, v123
	v_lshl_add_u32 v60, v124, 6, v1
	v_ashrrev_i32_e32 v1, 31, v0
	v_lshlrev_b64 v[0:1], 2, v[0:1]
	s_movk_i32 s4, 0xc00
	s_waitcnt lgkmcnt(0)
	v_lshl_add_u64 v[0:1], s[2:3], 0, v[0:1]
	v_mad_i64_i32 v[58:59], s[0:1], v60, s4, v[0:1]
	v_or_b32_e32 v50, 16, v60
	v_mad_i64_i32 v[52:53], s[0:1], v50, s4, v[0:1]
	v_or_b32_e32 v50, 32, v60
	v_mad_i64_i32 v[54:55], s[0:1], v50, s4, v[0:1]
	v_or_b32_e32 v50, 48, v60
	v_mad_i64_i32 v[56:57], s[0:1], v50, s4, v[0:1]
	s_waitcnt vmcnt(0)
	v_pk_add_f32 v[46:47], v[140:141], v[46:47]
	v_pk_add_f32 v[48:49], v[48:49], v[142:143]
	global_store_dwordx4 v[58:59], v[46:49], off
	v_pk_add_f32 v[42:43], v[144:145], v[42:43]
	v_pk_add_f32 v[44:45], v[44:45], v[146:147]
	global_store_dwordx4 v[58:59], v[42:45], off offset:64
	v_pk_add_f32 v[38:39], v[148:149], v[38:39]
	v_pk_add_f32 v[40:41], v[40:41], v[150:151]
	global_store_dwordx4 v[58:59], v[38:41], off offset:128
	v_pk_add_f32 v[34:35], v[152:153], v[34:35]
	v_pk_add_f32 v[36:37], v[36:37], v[154:155]
	global_store_dwordx4 v[52:53], v[34:37], off
	v_pk_add_f32 v[30:31], v[156:157], v[30:31]
	v_pk_add_f32 v[32:33], v[32:33], v[158:159]
	global_store_dwordx4 v[52:53], v[30:33], off offset:64
	v_pk_add_f32 v[26:27], v[160:161], v[26:27]
	v_pk_add_f32 v[28:29], v[28:29], v[162:163]
	global_store_dwordx4 v[52:53], v[26:29], off offset:128
	v_pk_add_f32 v[22:23], v[164:165], v[22:23]
	v_pk_add_f32 v[24:25], v[24:25], v[166:167]
	global_store_dwordx4 v[54:55], v[22:25], off
	v_pk_add_f32 v[18:19], v[168:169], v[18:19]
	v_pk_add_f32 v[20:21], v[20:21], v[170:171]
	global_store_dwordx4 v[54:55], v[18:21], off offset:64
	v_pk_add_f32 v[14:15], v[172:173], v[14:15]
	v_pk_add_f32 v[16:17], v[16:17], v[174:175]
	global_store_dwordx4 v[54:55], v[14:17], off offset:128
	v_pk_add_f32 v[10:11], v[176:177], v[10:11]
	v_pk_add_f32 v[12:13], v[12:13], v[178:179]
	global_store_dwordx4 v[56:57], v[10:13], off
	v_pk_add_f32 v[6:7], v[180:181], v[6:7]
	v_pk_add_f32 v[8:9], v[8:9], v[182:183]
	global_store_dwordx4 v[56:57], v[6:9], off offset:64
	v_pk_add_f32 v[2:3], v[184:185], v[2:3]
	v_pk_add_f32 v[4:5], v[4:5], v[186:187]
	global_store_dwordx4 v[56:57], v[2:5], off offset:128
	s_endpgm
	.p2align	8

	.amdhsa_kernel _Z7gemm128ILi3ELi96EEv8GemmArgs
		.amdhsa_group_segment_fixed_size 0
		.amdhsa_private_segment_fixed_size 0
		.amdhsa_kernarg_size 80
		.amdhsa_user_sgpr_count 2
		.amdhsa_user_sgpr_dispatch_ptr 0
		.amdhsa_user_sgpr_queue_ptr 0
		.amdhsa_user_sgpr_kernarg_segment_ptr 1
		.amdhsa_user_sgpr_dispatch_id 0
		.amdhsa_user_sgpr_kernarg_preload_length 0
		.amdhsa_user_sgpr_kernarg_preload_offset 0
		.amdhsa_user_sgpr_private_segment_size 0
		.amdhsa_uses_dynamic_stack 0
		.amdhsa_enable_private_segment 0
		.amdhsa_system_sgpr_workgroup_id_x 1
		.amdhsa_system_sgpr_workgroup_id_y 0
		.amdhsa_system_sgpr_workgroup_id_z 0
		.amdhsa_system_sgpr_workgroup_info 0
		.amdhsa_system_vgpr_workitem_id 0
		.amdhsa_next_free_vgpr 188
		.amdhsa_next_free_sgpr 19
		.amdhsa_accum_offset 188
		.amdhsa_reserve_vcc 1
		.amdhsa_float_round_mode_32 0
		.amdhsa_float_round_mode_16_64 0
		.amdhsa_float_denorm_mode_32 3
		.amdhsa_float_denorm_mode_16_64 3
		.amdhsa_dx10_clamp 1
		.amdhsa_ieee_mode 1
		.amdhsa_fp16_overflow 0
		.amdhsa_tg_split 0
		.amdhsa_exception_fp_ieee_invalid_op 0
		.amdhsa_exception_fp_denorm_src 0
		.amdhsa_exception_fp_ieee_div_zero 0
		.amdhsa_exception_fp_ieee_overflow 0
		.amdhsa_exception_fp_ieee_underflow 0
		.amdhsa_exception_fp_ieee_inexact 0
		.amdhsa_exception_int_div_zero 0
	.end_amdhsa_kernel

.Lfunc_end4:
	.size	_Z7gemm128ILi3ELi96EEv8GemmArgs, .Lfunc_end4-_Z7gemm128ILi3ELi96EEv8GemmArgs
	.set _Z7gemm128ILi3ELi96EEv8GemmArgs.num_vgpr, 188
	.set _Z7gemm128ILi3ELi96EEv8GemmArgs.num_agpr, 0
	.set _Z7gemm128ILi3ELi96EEv8GemmArgs.numbered_sgpr, 19
	.set _Z7gemm128ILi3ELi96EEv8GemmArgs.num_named_barrier, 0
	.set _Z7gemm128ILi3ELi96EEv8GemmArgs.private_seg_size, 0
	.set _Z7gemm128ILi3ELi96EEv8GemmArgs.uses_vcc, 1
	.set _Z7gemm128ILi3ELi96EEv8GemmArgs.uses_flat_scratch, 0
	.set _Z7gemm128ILi3ELi96EEv8GemmArgs.has_dyn_sized_stack, 0
	.set _Z7gemm128ILi3ELi96EEv8GemmArgs.has_recursion, 0
	.set _Z7gemm128ILi3ELi96EEv8GemmArgs.has_indirect_call, 0

.LBB6_8:
	s_lshl_b32 s0, s19, 8
	s_add_i32 s21, s21, s0
	v_or_b32_e32 v0, s21, v141
	v_mov_b32_e32 v1, 0
	v_lshlrev_b64 v[132:133], 6, v[0:1]
	s_waitcnt lgkmcnt(0)
	v_lshl_add_u64 v[132:133], s[10:11], 0, v[132:133]
	s_barrier
	global_load_dwordx4 v[134:137], v[132:133], off
	global_load_dwordx4 v[142:145], v[132:133], off offset:32
	global_load_dwordx4 v[146:149], v[132:133], off offset:16
	global_load_dwordx4 v[150:153], v[132:133], off offset:48
	s_lshl_b32 s1, s18, 8
	s_or_b32 s1, s7, s1
	v_or_b32_e32 v130, s1, v140
	v_mov_b32_e32 v132, s5
	v_mov_b32_e32 v129, v131
	s_mov_b32 s0, 0xc0135761
	v_mad_i64_i32 v[138:139], s[2:3], v0, s4, 0
	v_ashrrev_i32_e32 v131, 31, v130
	v_lshlrev_b64 v[130:131], 1, v[130:131]
	s_waitcnt vmcnt(0)
	v_mov_b32_e32 v140, v134
	v_mov_b32_e32 v141, v142
	v_mov_b32_e32 v142, v135
	v_mov_b32_e32 v134, v136
	v_mov_b32_e32 v135, v144
	v_mov_b32_e32 v144, v137
	v_mov_b32_e32 v136, v146
	v_mov_b32_e32 v137, v150
	v_mov_b32_e32 v150, v147
	v_mov_b32_e32 v146, v148
	v_mov_b32_e32 v147, v152
	v_mov_b32_e32 v152, v149
	v_pk_add_f32 v[140:141], v[140:141], v[142:143]
	v_pk_add_f32 v[134:135], v[134:135], v[144:145]
	v_pk_add_f32 v[136:137], v[136:137], v[150:151]
	v_pk_add_f32 v[142:143], v[146:147], v[152:153]
	v_pk_add_f32 v[134:135], v[140:141], v[134:135]
	v_pk_add_f32 v[136:137], v[136:137], v[142:143]
	s_nop 0
	v_pk_add_f32 v[134:135], v[134:135], v[136:137]
	v_lshl_add_u64 v[136:137], v[138:139], 1, s[8:9]
	v_add_f32_e32 v133, v134, v135
	v_fma_f32 v133, s6, v133, v132
	v_rsq_f32_e32 v134, v133
	v_lshl_add_u64 v[136:137], v[136:137], 0, v[130:131]
	v_pk_mul_f32 v[126:127], v[126:127], v[134:135] op_sel_hi:[1,0]
	v_pk_mul_f32 v[128:129], v[128:129], v[134:135] op_sel_hi:[1,0]
	v_pk_mul_f32 v[122:123], v[122:123], v[134:135] op_sel_hi:[1,0]
	v_pk_mul_f32 v[124:125], v[124:125], v[134:135] op_sel_hi:[1,0]
	v_pk_mul_f32 v[118:119], v[118:119], v[134:135] op_sel_hi:[1,0]
	v_mul_f32_e32 v133, 0x3dd2d3e8, v126
	v_mul_f32_e32 v135, 0x3dd2d3e8, v127
	v_mul_f32_e32 v138, 0x3dd2d3e8, v128
	v_mul_f32_e32 v139, 0x3dd2d3e8, v129
	v_mul_f32_e32 v140, 0x3dd2d3e8, v122
	v_mul_f32_e32 v141, 0x3dd2d3e8, v123
	v_fma_f32 v133, -v126, v133, s0
	v_fma_f32 v135, -v127, v135, s0
	v_mul_f32_e32 v142, 0x3dd2d3e8, v124
	v_mul_f32_e32 v143, 0x3dd2d3e8, v125
	v_fma_f32 v138, -v128, v138, s0
	v_fma_f32 v139, -v129, v139, s0
	v_fma_f32 v140, -v122, v140, s0
	v_fma_f32 v141, -v123, v141, s0
	v_mul_f32_e32 v133, v126, v133
	v_mul_f32_e32 v135, v127, v135
	v_fma_f32 v142, -v124, v142, s0
	v_fma_f32 v143, -v125, v143, s0
	v_mul_f32_e32 v138, v128, v138
	v_mul_f32_e32 v139, v129, v139
	v_mul_f32_e32 v140, v122, v140
	v_mul_f32_e32 v141, v123, v141
	v_exp_f32_e32 v133, v133
	v_exp_f32_e32 v135, v135
	v_mul_f32_e32 v142, v124, v142
	v_mul_f32_e32 v143, v125, v143
	v_exp_f32_e32 v138, v138
	v_exp_f32_e32 v139, v139
	v_exp_f32_e32 v140, v140
	v_exp_f32_e32 v141, v141
	v_mul_f32_e32 v144, 0x3dd2d3e8, v118
	v_exp_f32_e32 v142, v142
	v_exp_f32_e32 v143, v143
	v_fma_f32 v144, -v118, v144, s0
	v_mul_f32_e32 v144, v118, v144
	v_add_f32_e32 v133, 1.0, v133
	v_add_f32_e32 v135, 1.0, v135
	v_exp_f32_e32 v146, v144
	v_add_f32_e32 v144, 1.0, v138
	v_add_f32_e32 v145, 1.0, v139
	v_add_f32_e32 v147, 1.0, v140
	v_add_f32_e32 v148, 1.0, v141
	v_rcp_f32_e32 v138, v133
	v_rcp_f32_e32 v139, v135
	v_add_f32_e32 v149, 1.0, v142
	v_add_f32_e32 v150, 1.0, v143
	v_rcp_f32_e32 v142, v147
	v_rcp_f32_e32 v143, v148
	v_pk_mul_f32 v[126:127], v[126:127], v[138:139]
	v_rcp_f32_e32 v140, v144
	v_rcp_f32_e32 v141, v145
	v_pk_mul_f32 v[138:139], v[122:123], v[142:143]
	v_cvt_pk_bf16_f32 v122, v126, v127
	v_mul_f32_e32 v126, 0x3dd2d3e8, v119
	v_rcp_f32_e32 v144, v149
	v_rcp_f32_e32 v145, v150
	v_fma_f32 v126, -v119, v126, s0
	v_mul_f32_e32 v126, v119, v126
	v_exp_f32_e32 v126, v126
	v_pk_mul_f32 v[128:129], v[128:129], v[140:141]
	v_pk_mul_f32 v[140:141], v[124:125], v[144:145]
	v_cvt_pk_bf16_f32 v123, v128, v129
	v_cvt_pk_bf16_f32 v124, v138, v139
	v_cvt_pk_bf16_f32 v125, v140, v141
	v_pk_mul_f32 v[120:121], v[120:121], v[134:135] op_sel_hi:[1,0]
	v_pk_mul_f32 v[114:115], v[114:115], v[134:135] op_sel_hi:[1,0]
	v_pk_mul_f32 v[116:117], v[116:117], v[134:135] op_sel_hi:[1,0]
	global_store_dwordx4 v[136:137], v[122:125], off
	v_mul_f32_e32 v127, 0x3dd2d3e8, v115
	v_mul_f32_e32 v128, 0x3dd2d3e8, v116
	v_add_f32_e32 v123, 1.0, v126
	v_mul_f32_e32 v124, 0x3dd2d3e8, v120
	v_mul_f32_e32 v125, 0x3dd2d3e8, v121
	v_mul_f32_e32 v126, 0x3dd2d3e8, v114
	v_mul_f32_e32 v129, 0x3dd2d3e8, v117
	v_fma_f32 v124, -v120, v124, s0
	v_fma_f32 v125, -v121, v125, s0
	v_fma_f32 v126, -v114, v126, s0
	v_fma_f32 v127, -v115, v127, s0
	v_fma_f32 v128, -v116, v128, s0
	v_fma_f32 v129, -v117, v129, s0
	v_mul_f32_e32 v124, v120, v124
	v_mul_f32_e32 v125, v121, v125
	v_mul_f32_e32 v126, v114, v126
	v_mul_f32_e32 v127, v115, v127
	v_mul_f32_e32 v128, v116, v128
	v_mul_f32_e32 v129, v117, v129
	v_exp_f32_e32 v124, v124
	v_exp_f32_e32 v125, v125
	v_exp_f32_e32 v126, v126
	v_exp_f32_e32 v127, v127
	v_exp_f32_e32 v128, v128
	v_exp_f32_e32 v129, v129
	v_add_f32_e32 v122, 1.0, v146
	v_add_f32_e32 v124, 1.0, v124
	v_add_f32_e32 v125, 1.0, v125
	v_add_f32_e32 v126, 1.0, v126
	v_add_f32_e32 v127, 1.0, v127
	v_add_f32_e32 v128, 1.0, v128
	v_add_f32_e32 v129, 1.0, v129
	v_rcp_f32_e32 v122, v122
	v_rcp_f32_e32 v123, v123
	v_rcp_f32_e32 v124, v124
	v_rcp_f32_e32 v125, v125
	v_rcp_f32_e32 v126, v126
	v_rcp_f32_e32 v127, v127
	v_rcp_f32_e32 v128, v128
	v_rcp_f32_e32 v129, v129
	v_pk_mul_f32 v[118:119], v[118:119], v[122:123]
	v_pk_mul_f32 v[120:121], v[120:121], v[124:125]
	v_pk_mul_f32 v[122:123], v[114:115], v[126:127]
	v_pk_mul_f32 v[124:125], v[116:117], v[128:129]
	v_cvt_pk_bf16_f32 v114, v118, v119
	v_cvt_pk_bf16_f32 v115, v120, v121
	v_cvt_pk_bf16_f32 v116, v122, v123
	v_cvt_pk_bf16_f32 v117, v124, v125
	v_or_b32_e32 v134, 16, v0
	v_mov_b32_e32 v135, v1
	global_store_dwordx4 v[136:137], v[114:117], off offset:256
	s_nop 1
	v_lshlrev_b64 v[114:115], 6, v[134:135]
	v_lshl_add_u64 v[126:127], s[10:11], 0, v[114:115]
	global_load_dwordx4 v[114:117], v[126:127], off
	global_load_dwordx4 v[118:121], v[126:127], off offset:32
	global_load_dwordx4 v[122:125], v[126:127], off offset:16
	s_nop 0
	global_load_dwordx4 v[126:129], v[126:127], off offset:48
	s_waitcnt vmcnt(3)
	v_mov_b32_e32 v136, v114
	s_waitcnt vmcnt(2)
	v_mov_b32_e32 v137, v118
	v_mov_b32_e32 v118, v115
	v_mov_b32_e32 v114, v116
	v_mov_b32_e32 v115, v120
	v_mov_b32_e32 v120, v117
	s_waitcnt vmcnt(1)
	v_mov_b32_e32 v116, v122
	s_waitcnt vmcnt(0)
	v_mov_b32_e32 v117, v126
	v_mov_b32_e32 v126, v123
	v_mov_b32_e32 v122, v124
	v_mov_b32_e32 v123, v128
	v_mov_b32_e32 v128, v125
	v_pk_add_f32 v[118:119], v[136:137], v[118:119]
	v_pk_add_f32 v[114:115], v[114:115], v[120:121]
	v_pk_add_f32 v[116:117], v[116:117], v[126:127]
	v_pk_add_f32 v[120:121], v[122:123], v[128:129]
	v_pk_add_f32 v[114:115], v[118:119], v[114:115]
	v_pk_add_f32 v[116:117], v[116:117], v[120:121]
	s_nop 0
	v_pk_add_f32 v[114:115], v[114:115], v[116:117]
	v_mad_i64_i32 v[116:117], s[2:3], v134, s4, 0
	v_add_f32_e32 v114, v114, v115
	v_fma_f32 v114, s6, v114, v132
	v_rsq_f32_e32 v114, v114
	v_lshl_add_u64 v[116:117], v[116:117], 1, s[8:9]
	v_lshl_add_u64 v[116:117], v[116:117], 0, v[130:131]
	v_pk_mul_f32 v[110:111], v[110:111], v[114:115] op_sel_hi:[1,0]
	s_nop 0
	v_mul_f32_e32 v115, 0x3dd2d3e8, v110
	v_mul_f32_e32 v118, 0x3dd2d3e8, v111
	v_fma_f32 v115, -v110, v115, s0
	v_mul_f32_e32 v115, v110, v115
	v_fma_f32 v118, -v111, v118, s0
	v_exp_f32_e32 v115, v115
	v_mul_f32_e32 v118, v111, v118
	v_exp_f32_e32 v119, v118
	v_add_f32_e32 v115, 1.0, v115
	v_rcp_f32_e32 v118, v115
	v_add_f32_e32 v115, 1.0, v119
	v_pk_mul_f32 v[112:113], v[112:113], v[114:115] op_sel_hi:[1,0]
	s_nop 0
	v_mul_f32_e32 v119, 0x3dd2d3e8, v112
	v_fma_f32 v119, -v112, v119, s0
	v_mul_f32_e32 v119, v112, v119
	v_exp_f32_e32 v120, v119
	v_mul_f32_e32 v119, 0x3dd2d3e8, v113
	v_fma_f32 v119, -v113, v119, s0
	v_mul_f32_e32 v119, v113, v119
	v_exp_f32_e32 v121, v119
	v_rcp_f32_e32 v119, v115
	v_add_f32_e32 v115, 1.0, v120
	v_rcp_f32_e32 v120, v115
	v_add_f32_e32 v115, 1.0, v121
	v_pk_mul_f32 v[106:107], v[106:107], v[114:115] op_sel_hi:[1,0]
	v_pk_mul_f32 v[110:111], v[110:111], v[118:119]
	v_mul_f32_e32 v121, 0x3dd2d3e8, v106
	v_fma_f32 v121, -v106, v121, s0
	v_mul_f32_e32 v121, v106, v121
	v_exp_f32_e32 v122, v121
	v_mul_f32_e32 v121, 0x3dd2d3e8, v107
	v_fma_f32 v121, -v107, v121, s0
	v_mul_f32_e32 v121, v107, v121
	v_exp_f32_e32 v123, v121
	v_rcp_f32_e32 v121, v115
	v_add_f32_e32 v115, 1.0, v122
	v_rcp_f32_e32 v122, v115
	v_add_f32_e32 v115, 1.0, v123
	v_pk_mul_f32 v[108:109], v[108:109], v[114:115] op_sel_hi:[1,0]
	v_pk_mul_f32 v[112:113], v[112:113], v[120:121]
	v_mul_f32_e32 v123, 0x3dd2d3e8, v108
	v_fma_f32 v123, -v108, v123, s0
	v_mul_f32_e32 v123, v108, v123
	v_exp_f32_e32 v124, v123
	v_mul_f32_e32 v123, 0x3dd2d3e8, v109
	v_fma_f32 v123, -v109, v123, s0
	v_mul_f32_e32 v123, v109, v123
	v_exp_f32_e32 v125, v123
	v_rcp_f32_e32 v123, v115
	v_add_f32_e32 v115, 1.0, v124
	v_rcp_f32_e32 v124, v115
	v_add_f32_e32 v115, 1.0, v125
	v_pk_mul_f32 v[102:103], v[102:103], v[114:115] op_sel_hi:[1,0]
	v_pk_mul_f32 v[118:119], v[106:107], v[122:123]
	v_cvt_pk_bf16_f32 v106, v110, v111
	v_mul_f32_e32 v110, 0x3dd2d3e8, v102
	v_mul_f32_e32 v111, 0x3dd2d3e8, v103
	v_rcp_f32_e32 v125, v115
	v_fma_f32 v110, -v102, v110, s0
	v_fma_f32 v111, -v103, v111, s0
	v_mul_f32_e32 v110, v102, v110
	v_mul_f32_e32 v111, v103, v111
	v_exp_f32_e32 v110, v110
	v_exp_f32_e32 v111, v111
	v_pk_mul_f32 v[120:121], v[108:109], v[124:125]
	v_cvt_pk_bf16_f32 v107, v112, v113
	v_cvt_pk_bf16_f32 v108, v118, v119
	v_cvt_pk_bf16_f32 v109, v120, v121
	v_pk_mul_f32 v[104:105], v[104:105], v[114:115] op_sel_hi:[1,0]
	v_pk_mul_f32 v[98:99], v[98:99], v[114:115] op_sel_hi:[1,0]
	v_pk_mul_f32 v[100:101], v[100:101], v[114:115] op_sel_hi:[1,0]
	global_store_dwordx4 v[116:117], v[106:109], off
	v_mul_f32_e32 v112, 0x3dd2d3e8, v100
	v_mul_f32_e32 v113, 0x3dd2d3e8, v101
	v_add_f32_e32 v106, 1.0, v110
	v_add_f32_e32 v107, 1.0, v111
	v_mul_f32_e32 v108, 0x3dd2d3e8, v104
	v_mul_f32_e32 v109, 0x3dd2d3e8, v105
	v_mul_f32_e32 v110, 0x3dd2d3e8, v98
	v_mul_f32_e32 v111, 0x3dd2d3e8, v99
	v_fma_f32 v108, -v104, v108, s0
	v_fma_f32 v109, -v105, v109, s0
	v_fma_f32 v110, -v98, v110, s0
	v_fma_f32 v111, -v99, v111, s0
	v_fma_f32 v112, -v100, v112, s0
	v_fma_f32 v113, -v101, v113, s0
	v_mul_f32_e32 v108, v104, v108
	v_mul_f32_e32 v109, v105, v109
	v_mul_f32_e32 v110, v98, v110
	v_mul_f32_e32 v111, v99, v111
	v_mul_f32_e32 v112, v100, v112
	v_mul_f32_e32 v113, v101, v113
	v_exp_f32_e32 v108, v108
	v_exp_f32_e32 v109, v109
	v_exp_f32_e32 v110, v110
	v_exp_f32_e32 v111, v111
	v_exp_f32_e32 v112, v112
	v_exp_f32_e32 v113, v113
	v_add_f32_e32 v108, 1.0, v108
	v_add_f32_e32 v109, 1.0, v109
	v_add_f32_e32 v110, 1.0, v110
	v_add_f32_e32 v111, 1.0, v111
	v_add_f32_e32 v112, 1.0, v112
	v_add_f32_e32 v113, 1.0, v113
	v_rcp_f32_e32 v106, v106
	v_rcp_f32_e32 v107, v107
	v_rcp_f32_e32 v108, v108
	v_rcp_f32_e32 v109, v109
	v_rcp_f32_e32 v110, v110
	v_rcp_f32_e32 v111, v111
	v_rcp_f32_e32 v112, v112
	v_rcp_f32_e32 v113, v113
	v_pk_mul_f32 v[102:103], v[102:103], v[106:107]
	v_pk_mul_f32 v[104:105], v[104:105], v[108:109]
	v_pk_mul_f32 v[106:107], v[98:99], v[110:111]
	v_pk_mul_f32 v[108:109], v[100:101], v[112:113]
	v_cvt_pk_bf16_f32 v98, v102, v103
	v_cvt_pk_bf16_f32 v99, v104, v105
	v_cvt_pk_bf16_f32 v100, v106, v107
	v_cvt_pk_bf16_f32 v101, v108, v109
	v_or_b32_e32 v114, 32, v0
	v_mov_b32_e32 v115, v1
	global_store_dwordx4 v[116:117], v[98:101], off offset:256
	s_nop 1
	v_lshlrev_b64 v[98:99], 6, v[114:115]
	v_lshl_add_u64 v[116:117], s[10:11], 0, v[98:99]
	global_load_dwordx4 v[98:101], v[116:117], off
	global_load_dwordx4 v[102:105], v[116:117], off offset:32
	global_load_dwordx4 v[106:109], v[116:117], off offset:16
	global_load_dwordx4 v[110:113], v[116:117], off offset:48
	s_waitcnt vmcnt(3)
	v_mov_b32_e32 v116, v98
	s_waitcnt vmcnt(2)
	v_mov_b32_e32 v117, v102
	v_mov_b32_e32 v102, v99
	v_pk_add_f32 v[98:99], v[116:117], v[102:103]
	v_mov_b32_e32 v102, v100
	v_mov_b32_e32 v103, v104
	v_mov_b32_e32 v104, v101
	v_pk_add_f32 v[100:101], v[102:103], v[104:105]
	s_waitcnt vmcnt(1)
	v_mov_b32_e32 v102, v108
	v_pk_add_f32 v[98:99], v[98:99], v[100:101]
	v_mov_b32_e32 v100, v106
	s_waitcnt vmcnt(0)
	v_mov_b32_e32 v101, v110
	v_mov_b32_e32 v110, v107
	v_mov_b32_e32 v103, v112
	v_mov_b32_e32 v112, v109
	v_pk_add_f32 v[100:101], v[100:101], v[110:111]
	v_pk_add_f32 v[102:103], v[102:103], v[112:113]
	s_nop 0
	v_pk_add_f32 v[100:101], v[100:101], v[102:103]
	s_nop 0
	v_pk_add_f32 v[98:99], v[98:99], v[100:101]
	v_mad_i64_i32 v[100:101], s[2:3], v114, s4, 0
	v_add_f32_e32 v98, v98, v99
	v_fma_f32 v98, s6, v98, v132
	v_rsq_f32_e32 v98, v98
	v_lshl_add_u64 v[100:101], v[100:101], 1, s[8:9]
	v_lshl_add_u64 v[100:101], v[100:101], 0, v[130:131]
	v_pk_mul_f32 v[94:95], v[94:95], v[98:99] op_sel_hi:[1,0]
	s_nop 0
	v_mul_f32_e32 v99, 0x3dd2d3e8, v94
	v_fma_f32 v99, -v94, v99, s0
	v_mul_f32_e32 v102, 0x3dd2d3e8, v95
	v_mul_f32_e32 v99, v94, v99
	v_fma_f32 v102, -v95, v102, s0
	v_exp_f32_e32 v99, v99
	v_mul_f32_e32 v102, v95, v102
	v_exp_f32_e32 v103, v102
	v_add_f32_e32 v99, 1.0, v99
	v_rcp_f32_e32 v102, v99
	v_add_f32_e32 v99, 1.0, v103
	v_pk_mul_f32 v[96:97], v[96:97], v[98:99] op_sel_hi:[1,0]
	s_nop 0
	v_mul_f32_e32 v103, 0x3dd2d3e8, v96
	v_fma_f32 v103, -v96, v103, s0
	v_mul_f32_e32 v103, v96, v103
	v_exp_f32_e32 v104, v103
	v_mul_f32_e32 v103, 0x3dd2d3e8, v97
	v_fma_f32 v103, -v97, v103, s0
	v_mul_f32_e32 v103, v97, v103
	v_exp_f32_e32 v105, v103
	v_rcp_f32_e32 v103, v99
	v_add_f32_e32 v99, 1.0, v104
	v_rcp_f32_e32 v104, v99
	v_add_f32_e32 v99, 1.0, v105
	v_pk_mul_f32 v[90:91], v[90:91], v[98:99] op_sel_hi:[1,0]
	v_pk_mul_f32 v[94:95], v[94:95], v[102:103]
	v_mul_f32_e32 v105, 0x3dd2d3e8, v90
	v_fma_f32 v105, -v90, v105, s0
	v_mul_f32_e32 v105, v90, v105
	v_exp_f32_e32 v106, v105
	v_mul_f32_e32 v105, 0x3dd2d3e8, v91
	v_fma_f32 v105, -v91, v105, s0
	v_mul_f32_e32 v105, v91, v105
	v_exp_f32_e32 v107, v105
	v_rcp_f32_e32 v105, v99
	v_add_f32_e32 v99, 1.0, v106
	v_rcp_f32_e32 v106, v99
	v_add_f32_e32 v99, 1.0, v107
	v_pk_mul_f32 v[92:93], v[92:93], v[98:99] op_sel_hi:[1,0]
	v_pk_mul_f32 v[96:97], v[96:97], v[104:105]
	v_mul_f32_e32 v107, 0x3dd2d3e8, v92
	v_fma_f32 v107, -v92, v107, s0
	v_mul_f32_e32 v107, v92, v107
	v_exp_f32_e32 v108, v107
	v_mul_f32_e32 v107, 0x3dd2d3e8, v93
	v_fma_f32 v107, -v93, v107, s0
	v_mul_f32_e32 v107, v93, v107
	v_exp_f32_e32 v109, v107
	v_rcp_f32_e32 v107, v99
	v_add_f32_e32 v99, 1.0, v108
	v_rcp_f32_e32 v108, v99
	v_add_f32_e32 v99, 1.0, v109
	v_pk_mul_f32 v[86:87], v[86:87], v[98:99] op_sel_hi:[1,0]
	v_pk_mul_f32 v[102:103], v[90:91], v[106:107]
	v_cvt_pk_bf16_f32 v90, v94, v95
	v_mul_f32_e32 v94, 0x3dd2d3e8, v86
	v_mul_f32_e32 v95, 0x3dd2d3e8, v87
	v_rcp_f32_e32 v109, v99
	v_fma_f32 v94, -v86, v94, s0
	v_fma_f32 v95, -v87, v95, s0
	v_mul_f32_e32 v94, v86, v94
	v_mul_f32_e32 v95, v87, v95
	v_exp_f32_e32 v94, v94
	v_exp_f32_e32 v95, v95
	v_pk_mul_f32 v[104:105], v[92:93], v[108:109]
	v_cvt_pk_bf16_f32 v91, v96, v97
	v_cvt_pk_bf16_f32 v92, v102, v103
	v_cvt_pk_bf16_f32 v93, v104, v105
	v_pk_mul_f32 v[88:89], v[88:89], v[98:99] op_sel_hi:[1,0]
	v_pk_mul_f32 v[82:83], v[82:83], v[98:99] op_sel_hi:[1,0]
	v_pk_mul_f32 v[84:85], v[84:85], v[98:99] op_sel_hi:[1,0]
	global_store_dwordx4 v[100:101], v[90:93], off
	v_mul_f32_e32 v96, 0x3dd2d3e8, v84
	v_mul_f32_e32 v97, 0x3dd2d3e8, v85
	v_add_f32_e32 v90, 1.0, v94
	v_add_f32_e32 v91, 1.0, v95
	v_mul_f32_e32 v92, 0x3dd2d3e8, v88
	v_mul_f32_e32 v93, 0x3dd2d3e8, v89
	v_mul_f32_e32 v94, 0x3dd2d3e8, v82
	v_mul_f32_e32 v95, 0x3dd2d3e8, v83
	v_fma_f32 v92, -v88, v92, s0
	v_fma_f32 v93, -v89, v93, s0
	v_fma_f32 v94, -v82, v94, s0
	v_fma_f32 v95, -v83, v95, s0
	v_fma_f32 v96, -v84, v96, s0
	v_fma_f32 v97, -v85, v97, s0
	v_mul_f32_e32 v92, v88, v92
	v_mul_f32_e32 v93, v89, v93
	v_mul_f32_e32 v94, v82, v94
	v_mul_f32_e32 v95, v83, v95
	v_mul_f32_e32 v96, v84, v96
	v_mul_f32_e32 v97, v85, v97
	v_exp_f32_e32 v92, v92
	v_exp_f32_e32 v93, v93
	v_exp_f32_e32 v94, v94
	v_exp_f32_e32 v95, v95
	v_exp_f32_e32 v96, v96
	v_exp_f32_e32 v97, v97
	v_add_f32_e32 v92, 1.0, v92
	v_add_f32_e32 v93, 1.0, v93
	v_add_f32_e32 v94, 1.0, v94
	v_add_f32_e32 v95, 1.0, v95
	v_add_f32_e32 v96, 1.0, v96
	v_add_f32_e32 v97, 1.0, v97
	v_rcp_f32_e32 v90, v90
	v_rcp_f32_e32 v91, v91
	v_rcp_f32_e32 v92, v92
	v_rcp_f32_e32 v93, v93
	v_rcp_f32_e32 v94, v94
	v_rcp_f32_e32 v95, v95
	v_rcp_f32_e32 v96, v96
	v_rcp_f32_e32 v97, v97
	v_pk_mul_f32 v[86:87], v[86:87], v[90:91]
	v_pk_mul_f32 v[88:89], v[88:89], v[92:93]
	v_pk_mul_f32 v[90:91], v[82:83], v[94:95]
	v_pk_mul_f32 v[92:93], v[84:85], v[96:97]
	v_cvt_pk_bf16_f32 v82, v86, v87
	v_cvt_pk_bf16_f32 v83, v88, v89
	v_cvt_pk_bf16_f32 v84, v90, v91
	v_cvt_pk_bf16_f32 v85, v92, v93
	v_or_b32_e32 v98, 48, v0
	v_mov_b32_e32 v99, v1
	global_store_dwordx4 v[100:101], v[82:85], off offset:256
	s_nop 1
	v_lshlrev_b64 v[82:83], 6, v[98:99]
	v_lshl_add_u64 v[100:101], s[10:11], 0, v[82:83]
	global_load_dwordx4 v[82:85], v[100:101], off
	global_load_dwordx4 v[86:89], v[100:101], off offset:32
	global_load_dwordx4 v[90:93], v[100:101], off offset:16
	global_load_dwordx4 v[94:97], v[100:101], off offset:48
	s_waitcnt vmcnt(3)
	v_mov_b32_e32 v100, v82
	s_waitcnt vmcnt(2)
	v_mov_b32_e32 v101, v86
	v_mov_b32_e32 v86, v83
	v_pk_add_f32 v[82:83], v[100:101], v[86:87]
	v_mov_b32_e32 v86, v84
	v_mov_b32_e32 v87, v88
	v_mov_b32_e32 v88, v85
	v_pk_add_f32 v[84:85], v[86:87], v[88:89]
	s_waitcnt vmcnt(1)
	v_mov_b32_e32 v86, v92
	v_pk_add_f32 v[82:83], v[82:83], v[84:85]
	v_mov_b32_e32 v84, v90
	s_waitcnt vmcnt(0)
	v_mov_b32_e32 v85, v94
	v_mov_b32_e32 v94, v91
	v_mov_b32_e32 v87, v96
	v_mov_b32_e32 v96, v93
	v_pk_add_f32 v[84:85], v[84:85], v[94:95]
	v_pk_add_f32 v[86:87], v[86:87], v[96:97]
	s_nop 0
	v_pk_add_f32 v[84:85], v[84:85], v[86:87]
	s_nop 0
	v_pk_add_f32 v[82:83], v[82:83], v[84:85]
	v_mad_i64_i32 v[84:85], s[2:3], v98, s4, 0
	v_add_f32_e32 v82, v82, v83
	v_fma_f32 v82, s6, v82, v132
	v_rsq_f32_e32 v82, v82
	v_lshl_add_u64 v[84:85], v[84:85], 1, s[8:9]
	v_lshl_add_u64 v[84:85], v[84:85], 0, v[130:131]
	v_pk_mul_f32 v[78:79], v[78:79], v[82:83] op_sel_hi:[1,0]
	s_nop 0
	v_mul_f32_e32 v83, 0x3dd2d3e8, v78
	v_fma_f32 v83, -v78, v83, s0
	v_mul_f32_e32 v86, 0x3dd2d3e8, v79
	v_mul_f32_e32 v83, v78, v83
	v_fma_f32 v86, -v79, v86, s0
	v_exp_f32_e32 v83, v83
	v_mul_f32_e32 v86, v79, v86
	v_exp_f32_e32 v87, v86
	v_add_f32_e32 v83, 1.0, v83
	v_rcp_f32_e32 v86, v83
	v_add_f32_e32 v83, 1.0, v87
	v_pk_mul_f32 v[80:81], v[80:81], v[82:83] op_sel_hi:[1,0]
	s_nop 0
	v_mul_f32_e32 v87, 0x3dd2d3e8, v80
	v_fma_f32 v87, -v80, v87, s0
	v_mul_f32_e32 v87, v80, v87
	v_exp_f32_e32 v88, v87
	v_mul_f32_e32 v87, 0x3dd2d3e8, v81
	v_fma_f32 v87, -v81, v87, s0
	v_mul_f32_e32 v87, v81, v87
	v_exp_f32_e32 v89, v87
	v_rcp_f32_e32 v87, v83
	v_add_f32_e32 v83, 1.0, v88
	v_rcp_f32_e32 v88, v83
	v_add_f32_e32 v83, 1.0, v89
	v_pk_mul_f32 v[74:75], v[74:75], v[82:83] op_sel_hi:[1,0]
	v_pk_mul_f32 v[78:79], v[78:79], v[86:87]
	v_mul_f32_e32 v89, 0x3dd2d3e8, v74
	v_fma_f32 v89, -v74, v89, s0
	v_mul_f32_e32 v89, v74, v89
	v_exp_f32_e32 v90, v89
	v_mul_f32_e32 v89, 0x3dd2d3e8, v75
	v_fma_f32 v89, -v75, v89, s0
	v_mul_f32_e32 v89, v75, v89
	v_exp_f32_e32 v91, v89
	v_rcp_f32_e32 v89, v83
	v_add_f32_e32 v83, 1.0, v90
	v_rcp_f32_e32 v90, v83
	v_add_f32_e32 v83, 1.0, v91
	v_pk_mul_f32 v[76:77], v[76:77], v[82:83] op_sel_hi:[1,0]
	v_pk_mul_f32 v[80:81], v[80:81], v[88:89]
	v_mul_f32_e32 v91, 0x3dd2d3e8, v76
	v_fma_f32 v91, -v76, v91, s0
	v_mul_f32_e32 v91, v76, v91
	v_exp_f32_e32 v92, v91
	v_mul_f32_e32 v91, 0x3dd2d3e8, v77
	v_fma_f32 v91, -v77, v91, s0
	v_mul_f32_e32 v91, v77, v91
	v_exp_f32_e32 v93, v91
	v_rcp_f32_e32 v91, v83
	v_add_f32_e32 v83, 1.0, v92
	v_rcp_f32_e32 v92, v83
	v_add_f32_e32 v83, 1.0, v93
	v_pk_mul_f32 v[70:71], v[70:71], v[82:83] op_sel_hi:[1,0]
	v_pk_mul_f32 v[86:87], v[74:75], v[90:91]
	v_cvt_pk_bf16_f32 v74, v78, v79
	v_mul_f32_e32 v78, 0x3dd2d3e8, v70
	v_mul_f32_e32 v79, 0x3dd2d3e8, v71
	v_rcp_f32_e32 v93, v83
	v_fma_f32 v78, -v70, v78, s0
	v_fma_f32 v79, -v71, v79, s0
	v_mul_f32_e32 v78, v70, v78
	v_mul_f32_e32 v79, v71, v79
	v_exp_f32_e32 v78, v78
	v_exp_f32_e32 v79, v79
	v_pk_mul_f32 v[88:89], v[76:77], v[92:93]
	v_cvt_pk_bf16_f32 v75, v80, v81
	v_cvt_pk_bf16_f32 v76, v86, v87
	v_cvt_pk_bf16_f32 v77, v88, v89
	v_pk_mul_f32 v[72:73], v[72:73], v[82:83] op_sel_hi:[1,0]
	v_pk_mul_f32 v[66:67], v[66:67], v[82:83] op_sel_hi:[1,0]
	v_pk_mul_f32 v[68:69], v[68:69], v[82:83] op_sel_hi:[1,0]
	global_store_dwordx4 v[84:85], v[74:77], off
	v_mul_f32_e32 v80, 0x3dd2d3e8, v68
	v_mul_f32_e32 v81, 0x3dd2d3e8, v69
	v_add_f32_e32 v74, 1.0, v78
	v_add_f32_e32 v75, 1.0, v79
	v_mul_f32_e32 v76, 0x3dd2d3e8, v72
	v_mul_f32_e32 v77, 0x3dd2d3e8, v73
	v_mul_f32_e32 v78, 0x3dd2d3e8, v66
	v_mul_f32_e32 v79, 0x3dd2d3e8, v67
	v_fma_f32 v76, -v72, v76, s0
	v_fma_f32 v77, -v73, v77, s0
	v_fma_f32 v78, -v66, v78, s0
	v_fma_f32 v79, -v67, v79, s0
	v_fma_f32 v80, -v68, v80, s0
	v_fma_f32 v81, -v69, v81, s0
	v_mul_f32_e32 v76, v72, v76
	v_mul_f32_e32 v77, v73, v77
	v_mul_f32_e32 v78, v66, v78
	v_mul_f32_e32 v79, v67, v79
	v_mul_f32_e32 v80, v68, v80
	v_mul_f32_e32 v81, v69, v81
	v_exp_f32_e32 v76, v76
	v_exp_f32_e32 v77, v77
	v_exp_f32_e32 v78, v78
	v_exp_f32_e32 v79, v79
	v_exp_f32_e32 v80, v80
	v_exp_f32_e32 v81, v81
	v_add_f32_e32 v76, 1.0, v76
	v_add_f32_e32 v77, 1.0, v77
	v_add_f32_e32 v78, 1.0, v78
	v_add_f32_e32 v79, 1.0, v79
	v_add_f32_e32 v80, 1.0, v80
	v_add_f32_e32 v81, 1.0, v81
	v_rcp_f32_e32 v74, v74
	v_rcp_f32_e32 v75, v75
	v_rcp_f32_e32 v76, v76
	v_rcp_f32_e32 v77, v77
	v_rcp_f32_e32 v78, v78
	v_rcp_f32_e32 v79, v79
	v_rcp_f32_e32 v80, v80
	v_rcp_f32_e32 v81, v81
	v_pk_mul_f32 v[70:71], v[70:71], v[74:75]
	v_pk_mul_f32 v[72:73], v[72:73], v[76:77]
	v_pk_mul_f32 v[74:75], v[66:67], v[78:79]
	v_pk_mul_f32 v[76:77], v[68:69], v[80:81]
	v_cvt_pk_bf16_f32 v66, v70, v71
	v_cvt_pk_bf16_f32 v67, v72, v73
	v_cvt_pk_bf16_f32 v68, v74, v75
	v_cvt_pk_bf16_f32 v69, v76, v77
	v_add_u32_e32 v82, 0x80, v0
	v_mov_b32_e32 v83, v1
	global_store_dwordx4 v[84:85], v[66:69], off offset:256
	s_nop 1
	v_lshlrev_b64 v[66:67], 6, v[82:83]
	v_lshl_add_u64 v[84:85], s[10:11], 0, v[66:67]
	global_load_dwordx4 v[66:69], v[84:85], off
	global_load_dwordx4 v[70:73], v[84:85], off offset:32
	global_load_dwordx4 v[74:77], v[84:85], off offset:16
	global_load_dwordx4 v[78:81], v[84:85], off offset:48
	s_waitcnt vmcnt(3)
	v_mov_b32_e32 v84, v66
	s_waitcnt vmcnt(2)
	v_mov_b32_e32 v85, v70
	v_mov_b32_e32 v70, v67
	v_pk_add_f32 v[66:67], v[84:85], v[70:71]
	v_mov_b32_e32 v70, v68
	v_mov_b32_e32 v71, v72
	v_mov_b32_e32 v72, v69
	v_pk_add_f32 v[68:69], v[70:71], v[72:73]
	s_waitcnt vmcnt(1)
	v_mov_b32_e32 v70, v76
	v_pk_add_f32 v[66:67], v[66:67], v[68:69]
	v_mov_b32_e32 v68, v74
	s_waitcnt vmcnt(0)
	v_mov_b32_e32 v69, v78
	v_mov_b32_e32 v78, v75
	v_mov_b32_e32 v71, v80
	v_mov_b32_e32 v80, v77
	v_pk_add_f32 v[68:69], v[68:69], v[78:79]
	v_pk_add_f32 v[70:71], v[70:71], v[80:81]
	s_nop 0
	v_pk_add_f32 v[68:69], v[68:69], v[70:71]
	s_nop 0
	v_pk_add_f32 v[66:67], v[66:67], v[68:69]
	v_mad_i64_i32 v[68:69], s[2:3], v82, s4, 0
	v_add_f32_e32 v66, v66, v67
	v_fma_f32 v66, s6, v66, v132
	v_rsq_f32_e32 v66, v66
	v_lshl_add_u64 v[68:69], v[68:69], 1, s[8:9]
	v_lshl_add_u64 v[68:69], v[68:69], 0, v[130:131]
	v_pk_mul_f32 v[62:63], v[62:63], v[66:67] op_sel_hi:[1,0]
	s_nop 0
	v_mul_f32_e32 v67, 0x3dd2d3e8, v62
	v_fma_f32 v67, -v62, v67, s0
	v_mul_f32_e32 v70, 0x3dd2d3e8, v63
	v_mul_f32_e32 v67, v62, v67
	v_fma_f32 v70, -v63, v70, s0
	v_exp_f32_e32 v67, v67
	v_mul_f32_e32 v70, v63, v70
	v_exp_f32_e32 v71, v70
	v_add_f32_e32 v67, 1.0, v67
	v_rcp_f32_e32 v70, v67
	v_add_f32_e32 v67, 1.0, v71
	v_pk_mul_f32 v[64:65], v[64:65], v[66:67] op_sel_hi:[1,0]
	s_nop 0
	v_mul_f32_e32 v71, 0x3dd2d3e8, v64
	v_fma_f32 v71, -v64, v71, s0
	v_mul_f32_e32 v71, v64, v71
	v_exp_f32_e32 v72, v71
	v_mul_f32_e32 v71, 0x3dd2d3e8, v65
	v_fma_f32 v71, -v65, v71, s0
	v_mul_f32_e32 v71, v65, v71
	v_exp_f32_e32 v73, v71
	v_rcp_f32_e32 v71, v67
	v_add_f32_e32 v67, 1.0, v72
	v_rcp_f32_e32 v72, v67
	v_add_f32_e32 v67, 1.0, v73
	v_pk_mul_f32 v[58:59], v[58:59], v[66:67] op_sel_hi:[1,0]
	v_pk_mul_f32 v[62:63], v[62:63], v[70:71]
	v_mul_f32_e32 v73, 0x3dd2d3e8, v58
	v_fma_f32 v73, -v58, v73, s0
	v_mul_f32_e32 v73, v58, v73
	v_exp_f32_e32 v74, v73
	v_mul_f32_e32 v73, 0x3dd2d3e8, v59
	v_fma_f32 v73, -v59, v73, s0
	v_mul_f32_e32 v73, v59, v73
	v_exp_f32_e32 v75, v73
	v_rcp_f32_e32 v73, v67
	v_add_f32_e32 v67, 1.0, v74
	v_rcp_f32_e32 v74, v67
	v_add_f32_e32 v67, 1.0, v75
	v_pk_mul_f32 v[60:61], v[60:61], v[66:67] op_sel_hi:[1,0]
	v_pk_mul_f32 v[64:65], v[64:65], v[72:73]
	v_mul_f32_e32 v75, 0x3dd2d3e8, v60
	v_fma_f32 v75, -v60, v75, s0
	v_mul_f32_e32 v75, v60, v75
	v_exp_f32_e32 v76, v75
	v_mul_f32_e32 v75, 0x3dd2d3e8, v61
	v_fma_f32 v75, -v61, v75, s0
	v_mul_f32_e32 v75, v61, v75
	v_exp_f32_e32 v77, v75
	v_rcp_f32_e32 v75, v67
	v_add_f32_e32 v67, 1.0, v76
	v_rcp_f32_e32 v76, v67
	v_add_f32_e32 v67, 1.0, v77
	v_pk_mul_f32 v[54:55], v[54:55], v[66:67] op_sel_hi:[1,0]
	v_pk_mul_f32 v[70:71], v[58:59], v[74:75]
	v_cvt_pk_bf16_f32 v58, v62, v63
	v_mul_f32_e32 v62, 0x3dd2d3e8, v54
	v_mul_f32_e32 v63, 0x3dd2d3e8, v55
	v_rcp_f32_e32 v77, v67
	v_fma_f32 v62, -v54, v62, s0
	v_fma_f32 v63, -v55, v63, s0
	v_mul_f32_e32 v62, v54, v62
	v_mul_f32_e32 v63, v55, v63
	v_exp_f32_e32 v62, v62
	v_exp_f32_e32 v63, v63
	v_pk_mul_f32 v[72:73], v[60:61], v[76:77]
	v_cvt_pk_bf16_f32 v59, v64, v65
	v_cvt_pk_bf16_f32 v60, v70, v71
	v_cvt_pk_bf16_f32 v61, v72, v73
	v_pk_mul_f32 v[56:57], v[56:57], v[66:67] op_sel_hi:[1,0]
	v_pk_mul_f32 v[50:51], v[50:51], v[66:67] op_sel_hi:[1,0]
	v_pk_mul_f32 v[52:53], v[52:53], v[66:67] op_sel_hi:[1,0]
	global_store_dwordx4 v[68:69], v[58:61], off
	v_mul_f32_e32 v64, 0x3dd2d3e8, v52
	v_mul_f32_e32 v65, 0x3dd2d3e8, v53
	v_add_f32_e32 v58, 1.0, v62
	v_add_f32_e32 v59, 1.0, v63
	v_mul_f32_e32 v60, 0x3dd2d3e8, v56
	v_mul_f32_e32 v61, 0x3dd2d3e8, v57
	v_mul_f32_e32 v62, 0x3dd2d3e8, v50
	v_mul_f32_e32 v63, 0x3dd2d3e8, v51
	v_fma_f32 v60, -v56, v60, s0
	v_fma_f32 v61, -v57, v61, s0
	v_fma_f32 v62, -v50, v62, s0
	v_fma_f32 v63, -v51, v63, s0
	v_fma_f32 v64, -v52, v64, s0
	v_fma_f32 v65, -v53, v65, s0
	v_mul_f32_e32 v60, v56, v60
	v_mul_f32_e32 v61, v57, v61
	v_mul_f32_e32 v62, v50, v62
	v_mul_f32_e32 v63, v51, v63
	v_mul_f32_e32 v64, v52, v64
	v_mul_f32_e32 v65, v53, v65
	v_exp_f32_e32 v60, v60
	v_exp_f32_e32 v61, v61
	v_exp_f32_e32 v62, v62
	v_exp_f32_e32 v63, v63
	v_exp_f32_e32 v64, v64
	v_exp_f32_e32 v65, v65
	v_add_f32_e32 v60, 1.0, v60
	v_add_f32_e32 v61, 1.0, v61
	v_add_f32_e32 v62, 1.0, v62
	v_add_f32_e32 v63, 1.0, v63
	v_add_f32_e32 v64, 1.0, v64
	v_add_f32_e32 v65, 1.0, v65
	v_rcp_f32_e32 v58, v58
	v_rcp_f32_e32 v59, v59
	v_rcp_f32_e32 v60, v60
	v_rcp_f32_e32 v61, v61
	v_rcp_f32_e32 v62, v62
	v_rcp_f32_e32 v63, v63
	v_rcp_f32_e32 v64, v64
	v_rcp_f32_e32 v65, v65
	v_pk_mul_f32 v[54:55], v[54:55], v[58:59]
	v_pk_mul_f32 v[56:57], v[56:57], v[60:61]
	v_pk_mul_f32 v[58:59], v[50:51], v[62:63]
	v_pk_mul_f32 v[60:61], v[52:53], v[64:65]
	v_cvt_pk_bf16_f32 v50, v54, v55
	v_cvt_pk_bf16_f32 v51, v56, v57
	v_cvt_pk_bf16_f32 v52, v58, v59
	v_cvt_pk_bf16_f32 v53, v60, v61
	v_add_u32_e32 v66, 0x90, v0
	v_mov_b32_e32 v67, v1
	global_store_dwordx4 v[68:69], v[50:53], off offset:256
	s_nop 1
	v_lshlrev_b64 v[50:51], 6, v[66:67]
	v_lshl_add_u64 v[68:69], s[10:11], 0, v[50:51]
	global_load_dwordx4 v[50:53], v[68:69], off
	global_load_dwordx4 v[54:57], v[68:69], off offset:32
	global_load_dwordx4 v[58:61], v[68:69], off offset:16
	global_load_dwordx4 v[62:65], v[68:69], off offset:48
	s_waitcnt vmcnt(3)
	v_mov_b32_e32 v68, v50
	s_waitcnt vmcnt(2)
	v_mov_b32_e32 v69, v54
	v_mov_b32_e32 v54, v51
	v_pk_add_f32 v[50:51], v[68:69], v[54:55]
	v_mov_b32_e32 v54, v52
	v_mov_b32_e32 v55, v56
	v_mov_b32_e32 v56, v53
	v_pk_add_f32 v[52:53], v[54:55], v[56:57]
	s_waitcnt vmcnt(1)
	v_mov_b32_e32 v54, v60
	v_pk_add_f32 v[50:51], v[50:51], v[52:53]
	v_mov_b32_e32 v52, v58
	s_waitcnt vmcnt(0)
	v_mov_b32_e32 v53, v62
	v_mov_b32_e32 v62, v59
	v_mov_b32_e32 v55, v64
	v_mov_b32_e32 v64, v61
	v_pk_add_f32 v[52:53], v[52:53], v[62:63]
	v_pk_add_f32 v[54:55], v[54:55], v[64:65]
	s_nop 0
	v_pk_add_f32 v[52:53], v[52:53], v[54:55]
	s_nop 0
	v_pk_add_f32 v[50:51], v[50:51], v[52:53]
	v_mad_i64_i32 v[52:53], s[2:3], v66, s4, 0
	v_add_f32_e32 v50, v50, v51
	v_fma_f32 v50, s6, v50, v132
	v_rsq_f32_e32 v50, v50
	v_lshl_add_u64 v[52:53], v[52:53], 1, s[8:9]
	v_lshl_add_u64 v[52:53], v[52:53], 0, v[130:131]
	v_pk_mul_f32 v[46:47], v[46:47], v[50:51] op_sel_hi:[1,0]
	s_nop 0
	v_mul_f32_e32 v51, 0x3dd2d3e8, v46
	v_fma_f32 v51, -v46, v51, s0
	v_mul_f32_e32 v54, 0x3dd2d3e8, v47
	v_mul_f32_e32 v51, v46, v51
	v_fma_f32 v54, -v47, v54, s0
	v_exp_f32_e32 v51, v51
	v_mul_f32_e32 v54, v47, v54
	v_exp_f32_e32 v55, v54
	v_add_f32_e32 v51, 1.0, v51
	v_rcp_f32_e32 v54, v51
	v_add_f32_e32 v51, 1.0, v55
	v_pk_mul_f32 v[48:49], v[48:49], v[50:51] op_sel_hi:[1,0]
	s_nop 0
	v_mul_f32_e32 v55, 0x3dd2d3e8, v48
	v_fma_f32 v55, -v48, v55, s0
	v_mul_f32_e32 v55, v48, v55
	v_exp_f32_e32 v56, v55
	v_mul_f32_e32 v55, 0x3dd2d3e8, v49
	v_fma_f32 v55, -v49, v55, s0
	v_mul_f32_e32 v55, v49, v55
	v_exp_f32_e32 v57, v55
	v_rcp_f32_e32 v55, v51
	v_add_f32_e32 v51, 1.0, v56
	v_rcp_f32_e32 v56, v51
	v_add_f32_e32 v51, 1.0, v57
	v_pk_mul_f32 v[42:43], v[42:43], v[50:51] op_sel_hi:[1,0]
	v_pk_mul_f32 v[46:47], v[46:47], v[54:55]
	v_mul_f32_e32 v57, 0x3dd2d3e8, v42
	v_fma_f32 v57, -v42, v57, s0
	v_mul_f32_e32 v57, v42, v57
	v_exp_f32_e32 v58, v57
	v_mul_f32_e32 v57, 0x3dd2d3e8, v43
	v_fma_f32 v57, -v43, v57, s0
	v_mul_f32_e32 v57, v43, v57
	v_exp_f32_e32 v59, v57
	v_rcp_f32_e32 v57, v51
	v_add_f32_e32 v51, 1.0, v58
	v_rcp_f32_e32 v58, v51
	v_add_f32_e32 v51, 1.0, v59
	v_pk_mul_f32 v[44:45], v[44:45], v[50:51] op_sel_hi:[1,0]
	v_pk_mul_f32 v[48:49], v[48:49], v[56:57]
	v_mul_f32_e32 v59, 0x3dd2d3e8, v44
	v_fma_f32 v59, -v44, v59, s0
	v_mul_f32_e32 v59, v44, v59
	v_exp_f32_e32 v60, v59
	v_mul_f32_e32 v59, 0x3dd2d3e8, v45
	v_fma_f32 v59, -v45, v59, s0
	v_mul_f32_e32 v59, v45, v59
	v_exp_f32_e32 v61, v59
	v_rcp_f32_e32 v59, v51
	v_add_f32_e32 v51, 1.0, v60
	v_rcp_f32_e32 v60, v51
	v_add_f32_e32 v51, 1.0, v61
	v_pk_mul_f32 v[38:39], v[38:39], v[50:51] op_sel_hi:[1,0]
	v_pk_mul_f32 v[54:55], v[42:43], v[58:59]
	v_cvt_pk_bf16_f32 v42, v46, v47
	v_mul_f32_e32 v46, 0x3dd2d3e8, v38
	v_mul_f32_e32 v47, 0x3dd2d3e8, v39
	v_rcp_f32_e32 v61, v51
	v_fma_f32 v46, -v38, v46, s0
	v_fma_f32 v47, -v39, v47, s0
	v_mul_f32_e32 v46, v38, v46
	v_mul_f32_e32 v47, v39, v47
	v_exp_f32_e32 v46, v46
	v_exp_f32_e32 v47, v47
	v_pk_mul_f32 v[56:57], v[44:45], v[60:61]
	v_cvt_pk_bf16_f32 v43, v48, v49
	v_cvt_pk_bf16_f32 v44, v54, v55
	v_cvt_pk_bf16_f32 v45, v56, v57
	v_pk_mul_f32 v[40:41], v[40:41], v[50:51] op_sel_hi:[1,0]
	v_pk_mul_f32 v[34:35], v[34:35], v[50:51] op_sel_hi:[1,0]
	v_pk_mul_f32 v[36:37], v[36:37], v[50:51] op_sel_hi:[1,0]
	global_store_dwordx4 v[52:53], v[42:45], off
	v_mul_f32_e32 v48, 0x3dd2d3e8, v36
	v_mul_f32_e32 v49, 0x3dd2d3e8, v37
	v_add_f32_e32 v42, 1.0, v46
	v_add_f32_e32 v43, 1.0, v47
	v_mul_f32_e32 v44, 0x3dd2d3e8, v40
	v_mul_f32_e32 v45, 0x3dd2d3e8, v41
	v_mul_f32_e32 v46, 0x3dd2d3e8, v34
	v_mul_f32_e32 v47, 0x3dd2d3e8, v35
	v_fma_f32 v44, -v40, v44, s0
	v_fma_f32 v45, -v41, v45, s0
	v_fma_f32 v46, -v34, v46, s0
	v_fma_f32 v47, -v35, v47, s0
	v_fma_f32 v48, -v36, v48, s0
	v_fma_f32 v49, -v37, v49, s0
	v_mul_f32_e32 v44, v40, v44
	v_mul_f32_e32 v45, v41, v45
	v_mul_f32_e32 v46, v34, v46
	v_mul_f32_e32 v47, v35, v47
	v_mul_f32_e32 v48, v36, v48
	v_mul_f32_e32 v49, v37, v49
	v_exp_f32_e32 v44, v44
	v_exp_f32_e32 v45, v45
	v_exp_f32_e32 v46, v46
	v_exp_f32_e32 v47, v47
	v_exp_f32_e32 v48, v48
	v_exp_f32_e32 v49, v49
	v_add_f32_e32 v44, 1.0, v44
	v_add_f32_e32 v45, 1.0, v45
	v_add_f32_e32 v46, 1.0, v46
	v_add_f32_e32 v47, 1.0, v47
	v_add_f32_e32 v48, 1.0, v48
	v_add_f32_e32 v49, 1.0, v49
	v_rcp_f32_e32 v42, v42
	v_rcp_f32_e32 v43, v43
	v_rcp_f32_e32 v44, v44
	v_rcp_f32_e32 v45, v45
	v_rcp_f32_e32 v46, v46
	v_rcp_f32_e32 v47, v47
	v_rcp_f32_e32 v48, v48
	v_rcp_f32_e32 v49, v49
	v_pk_mul_f32 v[38:39], v[38:39], v[42:43]
	v_pk_mul_f32 v[40:41], v[40:41], v[44:45]
	v_pk_mul_f32 v[42:43], v[34:35], v[46:47]
	v_pk_mul_f32 v[44:45], v[36:37], v[48:49]
	v_cvt_pk_bf16_f32 v34, v38, v39
	v_cvt_pk_bf16_f32 v35, v40, v41
	v_cvt_pk_bf16_f32 v36, v42, v43
	v_cvt_pk_bf16_f32 v37, v44, v45
	v_add_u32_e32 v50, 0xa0, v0
	v_mov_b32_e32 v51, v1
	global_store_dwordx4 v[52:53], v[34:37], off offset:256
	v_add_u32_e32 v0, 0xb0, v0
	s_nop 0
	v_lshlrev_b64 v[34:35], 6, v[50:51]
	v_lshl_add_u64 v[52:53], s[10:11], 0, v[34:35]
	global_load_dwordx4 v[34:37], v[52:53], off
	global_load_dwordx4 v[38:41], v[52:53], off offset:32
	global_load_dwordx4 v[42:45], v[52:53], off offset:16
	global_load_dwordx4 v[46:49], v[52:53], off offset:48
	s_waitcnt vmcnt(3)
	v_mov_b32_e32 v52, v34
	s_waitcnt vmcnt(2)
	v_mov_b32_e32 v53, v38
	v_mov_b32_e32 v38, v35
	v_pk_add_f32 v[34:35], v[52:53], v[38:39]
	v_mov_b32_e32 v38, v36
	v_mov_b32_e32 v39, v40
	v_mov_b32_e32 v40, v37
	v_pk_add_f32 v[36:37], v[38:39], v[40:41]
	s_waitcnt vmcnt(1)
	v_mov_b32_e32 v38, v44
	v_pk_add_f32 v[34:35], v[34:35], v[36:37]
	v_mov_b32_e32 v36, v42
	s_waitcnt vmcnt(0)
	v_mov_b32_e32 v37, v46
	v_mov_b32_e32 v46, v43
	v_mov_b32_e32 v39, v48
	v_mov_b32_e32 v48, v45
	v_pk_add_f32 v[36:37], v[36:37], v[46:47]
	v_pk_add_f32 v[38:39], v[38:39], v[48:49]
	s_nop 0
	v_pk_add_f32 v[36:37], v[36:37], v[38:39]
	s_nop 0
	v_pk_add_f32 v[34:35], v[34:35], v[36:37]
	v_mad_i64_i32 v[36:37], s[2:3], v50, s4, 0
	v_add_f32_e32 v34, v34, v35
	v_fma_f32 v34, s6, v34, v132
	v_rsq_f32_e32 v34, v34
	v_lshl_add_u64 v[36:37], v[36:37], 1, s[8:9]
	v_lshl_add_u64 v[36:37], v[36:37], 0, v[130:131]
	v_pk_mul_f32 v[30:31], v[30:31], v[34:35] op_sel_hi:[1,0]
	s_nop 0
	v_mul_f32_e32 v35, 0x3dd2d3e8, v30
	v_fma_f32 v35, -v30, v35, s0
	v_mul_f32_e32 v38, 0x3dd2d3e8, v31
	v_mul_f32_e32 v35, v30, v35
	v_fma_f32 v38, -v31, v38, s0
	v_exp_f32_e32 v35, v35
	v_mul_f32_e32 v38, v31, v38
	v_exp_f32_e32 v39, v38
	v_add_f32_e32 v35, 1.0, v35
	v_rcp_f32_e32 v38, v35
	v_add_f32_e32 v35, 1.0, v39
	v_pk_mul_f32 v[32:33], v[32:33], v[34:35] op_sel_hi:[1,0]
	s_nop 0
	v_mul_f32_e32 v39, 0x3dd2d3e8, v32
	v_fma_f32 v39, -v32, v39, s0
	v_mul_f32_e32 v39, v32, v39
	v_exp_f32_e32 v40, v39
	v_mul_f32_e32 v39, 0x3dd2d3e8, v33
	v_fma_f32 v39, -v33, v39, s0
	v_mul_f32_e32 v39, v33, v39
	v_exp_f32_e32 v41, v39
	v_rcp_f32_e32 v39, v35
	v_add_f32_e32 v35, 1.0, v40
	v_rcp_f32_e32 v40, v35
	v_add_f32_e32 v35, 1.0, v41
	v_pk_mul_f32 v[26:27], v[26:27], v[34:35] op_sel_hi:[1,0]
	v_pk_mul_f32 v[30:31], v[30:31], v[38:39]
	v_mul_f32_e32 v41, 0x3dd2d3e8, v26
	v_fma_f32 v41, -v26, v41, s0
	v_mul_f32_e32 v41, v26, v41
	v_exp_f32_e32 v42, v41
	v_mul_f32_e32 v41, 0x3dd2d3e8, v27
	v_fma_f32 v41, -v27, v41, s0
	v_mul_f32_e32 v41, v27, v41
	v_exp_f32_e32 v43, v41
	v_rcp_f32_e32 v41, v35
	v_add_f32_e32 v35, 1.0, v42
	v_rcp_f32_e32 v42, v35
	v_add_f32_e32 v35, 1.0, v43
	v_pk_mul_f32 v[28:29], v[28:29], v[34:35] op_sel_hi:[1,0]
	v_pk_mul_f32 v[32:33], v[32:33], v[40:41]
	v_mul_f32_e32 v43, 0x3dd2d3e8, v28
	v_fma_f32 v43, -v28, v43, s0
	v_mul_f32_e32 v43, v28, v43
	v_exp_f32_e32 v44, v43
	v_mul_f32_e32 v43, 0x3dd2d3e8, v29
	v_fma_f32 v43, -v29, v43, s0
	v_mul_f32_e32 v43, v29, v43
	v_exp_f32_e32 v45, v43
	v_rcp_f32_e32 v43, v35
	v_add_f32_e32 v35, 1.0, v44
	v_rcp_f32_e32 v44, v35
	v_add_f32_e32 v35, 1.0, v45
	v_pk_mul_f32 v[22:23], v[22:23], v[34:35] op_sel_hi:[1,0]
	v_pk_mul_f32 v[38:39], v[26:27], v[42:43]
	v_cvt_pk_bf16_f32 v26, v30, v31
	v_mul_f32_e32 v30, 0x3dd2d3e8, v22
	v_mul_f32_e32 v31, 0x3dd2d3e8, v23
	v_rcp_f32_e32 v45, v35
	v_fma_f32 v30, -v22, v30, s0
	v_fma_f32 v31, -v23, v31, s0
	v_mul_f32_e32 v30, v22, v30
	v_mul_f32_e32 v31, v23, v31
	v_exp_f32_e32 v30, v30
	v_exp_f32_e32 v31, v31
	v_pk_mul_f32 v[40:41], v[28:29], v[44:45]
	v_cvt_pk_bf16_f32 v27, v32, v33
	v_cvt_pk_bf16_f32 v28, v38, v39
	v_cvt_pk_bf16_f32 v29, v40, v41
	v_pk_mul_f32 v[24:25], v[24:25], v[34:35] op_sel_hi:[1,0]
	v_pk_mul_f32 v[18:19], v[18:19], v[34:35] op_sel_hi:[1,0]
	v_pk_mul_f32 v[20:21], v[20:21], v[34:35] op_sel_hi:[1,0]
	global_store_dwordx4 v[36:37], v[26:29], off
	v_mul_f32_e32 v32, 0x3dd2d3e8, v20
	v_mul_f32_e32 v33, 0x3dd2d3e8, v21
	v_add_f32_e32 v26, 1.0, v30
	v_add_f32_e32 v27, 1.0, v31
	v_mul_f32_e32 v28, 0x3dd2d3e8, v24
	v_mul_f32_e32 v29, 0x3dd2d3e8, v25
	v_mul_f32_e32 v30, 0x3dd2d3e8, v18
	v_mul_f32_e32 v31, 0x3dd2d3e8, v19
	v_fma_f32 v28, -v24, v28, s0
	v_fma_f32 v29, -v25, v29, s0
	v_fma_f32 v30, -v18, v30, s0
	v_fma_f32 v31, -v19, v31, s0
	v_fma_f32 v32, -v20, v32, s0
	v_fma_f32 v33, -v21, v33, s0
	v_mul_f32_e32 v28, v24, v28
	v_mul_f32_e32 v29, v25, v29
	v_mul_f32_e32 v30, v18, v30
	v_mul_f32_e32 v31, v19, v31
	v_mul_f32_e32 v32, v20, v32
	v_mul_f32_e32 v33, v21, v33
	v_exp_f32_e32 v28, v28
	v_exp_f32_e32 v29, v29
	v_exp_f32_e32 v30, v30
	v_exp_f32_e32 v31, v31
	v_exp_f32_e32 v32, v32
	v_exp_f32_e32 v33, v33
	v_add_f32_e32 v28, 1.0, v28
	v_add_f32_e32 v29, 1.0, v29
	v_add_f32_e32 v30, 1.0, v30
	v_add_f32_e32 v31, 1.0, v31
	v_add_f32_e32 v32, 1.0, v32
	v_add_f32_e32 v33, 1.0, v33
	v_rcp_f32_e32 v26, v26
	v_rcp_f32_e32 v27, v27
	v_rcp_f32_e32 v28, v28
	v_rcp_f32_e32 v29, v29
	v_rcp_f32_e32 v30, v30
	v_rcp_f32_e32 v31, v31
	v_rcp_f32_e32 v32, v32
	v_rcp_f32_e32 v33, v33
	v_pk_mul_f32 v[22:23], v[22:23], v[26:27]
	v_pk_mul_f32 v[24:25], v[24:25], v[28:29]
	v_pk_mul_f32 v[26:27], v[18:19], v[30:31]
	v_pk_mul_f32 v[28:29], v[20:21], v[32:33]
	v_cvt_pk_bf16_f32 v18, v22, v23
	v_cvt_pk_bf16_f32 v19, v24, v25
	v_cvt_pk_bf16_f32 v20, v26, v27
	v_cvt_pk_bf16_f32 v21, v28, v29
	global_store_dwordx4 v[36:37], v[18:21], off offset:256
	s_nop 1
	v_lshlrev_b64 v[18:19], 6, v[0:1]
	v_lshl_add_u64 v[34:35], s[10:11], 0, v[18:19]
	global_load_dwordx4 v[18:21], v[34:35], off
	global_load_dwordx4 v[22:25], v[34:35], off offset:32
	global_load_dwordx4 v[26:29], v[34:35], off offset:16
	global_load_dwordx4 v[30:33], v[34:35], off offset:48
	s_waitcnt vmcnt(3)
	v_mov_b32_e32 v34, v18
	s_waitcnt vmcnt(2)
	v_mov_b32_e32 v35, v22
	v_mov_b32_e32 v22, v19
	v_pk_add_f32 v[18:19], v[34:35], v[22:23]
	v_mov_b32_e32 v22, v20
	v_mov_b32_e32 v23, v24
	v_mov_b32_e32 v24, v21
	v_pk_add_f32 v[20:21], v[22:23], v[24:25]
	s_waitcnt vmcnt(1)
	v_mov_b32_e32 v22, v28
	v_pk_add_f32 v[18:19], v[18:19], v[20:21]
	v_mov_b32_e32 v20, v26
	s_waitcnt vmcnt(0)
	v_mov_b32_e32 v21, v30
	v_mov_b32_e32 v30, v27
	v_mov_b32_e32 v23, v32
	v_mov_b32_e32 v32, v29
	v_pk_add_f32 v[20:21], v[20:21], v[30:31]
	v_pk_add_f32 v[22:23], v[22:23], v[32:33]
	s_nop 0
	v_pk_add_f32 v[20:21], v[20:21], v[22:23]
	s_nop 0
	v_pk_add_f32 v[18:19], v[18:19], v[20:21]
	s_nop 0
	v_add_f32_e32 v1, v18, v19
	v_fma_f32 v1, s6, v1, v132
	v_rsq_f32_e32 v18, v1
	v_mad_i64_i32 v[0:1], s[2:3], v0, s4, 0
	v_lshl_add_u64 v[0:1], v[0:1], 1, s[8:9]
	v_pk_mul_f32 v[14:15], v[14:15], v[18:19] op_sel_hi:[1,0]
	s_nop 0
	v_mul_f32_e32 v19, 0x3dd2d3e8, v14
	v_fma_f32 v19, -v14, v19, s0
	v_mul_f32_e32 v19, v14, v19
	v_mul_f32_e32 v20, 0x3dd2d3e8, v15
	v_exp_f32_e32 v19, v19
	v_fma_f32 v20, -v15, v20, s0
	v_mul_f32_e32 v20, v15, v20
	v_exp_f32_e32 v22, v20
	v_pk_mul_f32 v[16:17], v[16:17], v[18:19] op_sel_hi:[1,0]
	v_lshl_add_u64 v[20:21], v[0:1], 0, v[130:131]
	v_add_f32_e32 v0, 1.0, v19
	v_mul_f32_e32 v19, 0x3dd2d3e8, v16
	v_add_f32_e32 v1, 1.0, v22
	v_fma_f32 v19, -v16, v19, s0
	v_mul_f32_e32 v22, 0x3dd2d3e8, v17
	v_mul_f32_e32 v19, v16, v19
	v_fma_f32 v22, -v17, v22, s0
	v_exp_f32_e32 v19, v19
	v_mul_f32_e32 v22, v17, v22
	v_exp_f32_e32 v23, v22
	v_rcp_f32_e32 v0, v0
	v_add_f32_e32 v19, 1.0, v19
	v_rcp_f32_e32 v22, v19
	v_add_f32_e32 v19, 1.0, v23
	v_pk_mul_f32 v[10:11], v[10:11], v[18:19] op_sel_hi:[1,0]
	v_rcp_f32_e32 v1, v1
	v_mul_f32_e32 v23, 0x3dd2d3e8, v10
	v_fma_f32 v23, -v10, v23, s0
	v_mul_f32_e32 v23, v10, v23
	v_exp_f32_e32 v24, v23
	v_mul_f32_e32 v23, 0x3dd2d3e8, v11
	v_fma_f32 v23, -v11, v23, s0
	v_mul_f32_e32 v23, v11, v23
	v_exp_f32_e32 v25, v23
	v_rcp_f32_e32 v23, v19
	v_add_f32_e32 v19, 1.0, v24
	v_rcp_f32_e32 v24, v19
	v_add_f32_e32 v19, 1.0, v25
	v_pk_mul_f32 v[12:13], v[12:13], v[18:19] op_sel_hi:[1,0]
	v_pk_mul_f32 v[0:1], v[14:15], v[0:1]
	v_mul_f32_e32 v25, 0x3dd2d3e8, v12
	v_fma_f32 v25, -v12, v25, s0
	v_mul_f32_e32 v25, v12, v25
	v_exp_f32_e32 v26, v25
	v_mul_f32_e32 v25, 0x3dd2d3e8, v13
	v_fma_f32 v25, -v13, v25, s0
	v_mul_f32_e32 v25, v13, v25
	v_exp_f32_e32 v27, v25
	v_rcp_f32_e32 v25, v19
	v_add_f32_e32 v19, 1.0, v26
	v_rcp_f32_e32 v26, v19
	v_add_f32_e32 v19, 1.0, v27
	v_rcp_f32_e32 v27, v19
	v_pk_mul_f32 v[14:15], v[16:17], v[22:23]
	v_pk_mul_f32 v[16:17], v[10:11], v[24:25]
	v_cvt_pk_bf16_f32 v10, v0, v1
	v_pk_mul_f32 v[22:23], v[12:13], v[26:27]
	v_cvt_pk_bf16_f32 v11, v14, v15
	v_cvt_pk_bf16_f32 v12, v16, v17
	v_cvt_pk_bf16_f32 v13, v22, v23
	v_pk_mul_f32 v[0:1], v[6:7], v[18:19] op_sel_hi:[1,0]
	v_pk_mul_f32 v[8:9], v[8:9], v[18:19] op_sel_hi:[1,0]
	v_pk_mul_f32 v[2:3], v[2:3], v[18:19] op_sel_hi:[1,0]
	v_pk_mul_f32 v[4:5], v[4:5], v[18:19] op_sel_hi:[1,0]
	v_mul_f32_e32 v6, 0x3dd2d3e8, v0
	v_mul_f32_e32 v7, 0x3dd2d3e8, v1
	global_store_dwordx4 v[20:21], v[10:13], off
	v_mul_f32_e32 v14, 0x3dd2d3e8, v4
	v_mul_f32_e32 v15, 0x3dd2d3e8, v5
	v_mul_f32_e32 v10, 0x3dd2d3e8, v8
	v_mul_f32_e32 v11, 0x3dd2d3e8, v9
	v_mul_f32_e32 v12, 0x3dd2d3e8, v2
	v_mul_f32_e32 v13, 0x3dd2d3e8, v3
	v_fma_f32 v6, -v0, v6, s0
	v_fma_f32 v7, -v1, v7, s0
	v_fma_f32 v10, -v8, v10, s0
	v_fma_f32 v11, -v9, v11, s0
	v_fma_f32 v12, -v2, v12, s0
	v_fma_f32 v13, -v3, v13, s0
	v_fma_f32 v14, -v4, v14, s0
	v_fma_f32 v15, -v5, v15, s0
	v_mul_f32_e32 v6, v0, v6
	v_mul_f32_e32 v7, v1, v7
	v_mul_f32_e32 v10, v8, v10
	v_mul_f32_e32 v11, v9, v11
	v_mul_f32_e32 v12, v2, v12
	v_mul_f32_e32 v13, v3, v13
	v_mul_f32_e32 v14, v4, v14
	v_mul_f32_e32 v15, v5, v15
	v_exp_f32_e32 v6, v6
	v_exp_f32_e32 v7, v7
	v_exp_f32_e32 v10, v10
	v_exp_f32_e32 v11, v11
	v_exp_f32_e32 v12, v12
	v_exp_f32_e32 v13, v13
	v_exp_f32_e32 v14, v14
	v_exp_f32_e32 v15, v15
	v_add_f32_e32 v6, 1.0, v6
	v_add_f32_e32 v7, 1.0, v7
	v_add_f32_e32 v10, 1.0, v10
	v_add_f32_e32 v11, 1.0, v11
	v_add_f32_e32 v12, 1.0, v12
	v_add_f32_e32 v13, 1.0, v13
	v_add_f32_e32 v14, 1.0, v14
	v_add_f32_e32 v15, 1.0, v15
	v_rcp_f32_e32 v6, v6
	v_rcp_f32_e32 v7, v7
	v_rcp_f32_e32 v10, v10
	v_rcp_f32_e32 v11, v11
	v_rcp_f32_e32 v12, v12
	v_rcp_f32_e32 v13, v13
	v_rcp_f32_e32 v14, v14
	v_rcp_f32_e32 v15, v15
	v_pk_mul_f32 v[0:1], v[0:1], v[6:7]
	v_pk_mul_f32 v[6:7], v[8:9], v[10:11]
	v_pk_mul_f32 v[2:3], v[2:3], v[12:13]
	v_pk_mul_f32 v[4:5], v[4:5], v[14:15]
	v_cvt_pk_bf16_f32 v0, v0, v1
	v_cvt_pk_bf16_f32 v1, v6, v7
	v_cvt_pk_bf16_f32 v2, v2, v3
	v_cvt_pk_bf16_f32 v3, v4, v5
	global_store_dwordx4 v[20:21], v[0:3], off offset:256
	s_endpgm
	.p2align	8

amdhsa.kernels:
  - .agpr_count:     0
    .args:
      - .offset:         0
        .size:           136
        .value_kind:     by_value
      - .offset:         136
        .size:           4
        .value_kind:     hidden_block_count_x
      - .offset:         140
        .size:           4
        .value_kind:     hidden_block_count_y
      - .offset:         144
        .size:           4
        .value_kind:     hidden_block_count_z
      - .offset:         148
        .size:           2
        .value_kind:     hidden_group_size_x
      - .offset:         150
        .size:           2
        .value_kind:     hidden_group_size_y
      - .offset:         152
        .size:           2
        .value_kind:     hidden_group_size_z
      - .offset:         154
        .size:           2
        .value_kind:     hidden_remainder_x
      - .offset:         156
        .size:           2
        .value_kind:     hidden_remainder_y
      - .offset:         158
        .size:           2
        .value_kind:     hidden_remainder_z
      - .offset:         176
        .size:           8
        .value_kind:     hidden_global_offset_x
      - .offset:         184
        .size:           8
        .value_kind:     hidden_global_offset_y
      - .offset:         192
        .size:           8
        .value_kind:     hidden_global_offset_z
      - .offset:         200
        .size:           2
        .value_kind:     hidden_grid_dims
    .group_segment_fixed_size: 16640
    .kernarg_segment_align: 8
    .kernarg_segment_size: 392
    .language:       OpenCL C
    .language_version:
      - 2
      - 0
    .max_flat_workgroup_size: 256
    .name:           _Z11prep_kernel8PrepArgs
    .private_segment_fixed_size: 0
    .sgpr_count:     26
    .sgpr_spill_count: 0
    .symbol:         _Z11prep_kernel8PrepArgs.kd
    .uniform_work_group_size: 1
    .uses_dynamic_stack: false
    .vgpr_count:     46
    .vgpr_spill_count: 0
    .wavefront_size: 64
  - .agpr_count:     0
    .args:
      - .offset:         0
        .size:           216
        .value_kind:     by_value
    .group_segment_fixed_size: 0
    .kernarg_segment_align: 8
    .kernarg_segment_size: 216
    .language:       OpenCL C
    .language_version:
      - 2
      - 0
    .max_flat_workgroup_size: 512
    .name:           _Z11attn_kernel8AttnArgs
    .private_segment_fixed_size: 0
    .sgpr_count:     82
    .sgpr_spill_count: 0
    .symbol:         _Z11attn_kernel8AttnArgs.kd
    .uniform_work_group_size: 1
    .uses_dynamic_stack: false
    .vgpr_count:     220
    .vgpr_spill_count: 0
    .wavefront_size: 64
  - .agpr_count:     0
    .args:
      - .offset:         0
        .size:           80
        .value_kind:     by_value
    .group_segment_fixed_size: 0
    .kernarg_segment_align: 8
    .kernarg_segment_size: 80
    .language:       OpenCL C
    .language_version:
      - 2
      - 0
    .max_flat_workgroup_size: 256
    .name:           _Z7gemm128ILi1ELi96EEv8GemmArgs
    .private_segment_fixed_size: 0
    .sgpr_count:     26
    .sgpr_spill_count: 0
    .symbol:         _Z7gemm128ILi1ELi96EEv8GemmArgs.kd
    .uniform_work_group_size: 1
    .uses_dynamic_stack: false
    .vgpr_count:     141
    .vgpr_spill_count: 0
    .wavefront_size: 64
  - .agpr_count:     0
    .args:
      - .offset:         0
        .size:           80
        .value_kind:     by_value
    .group_segment_fixed_size: 0
    .kernarg_segment_align: 8
    .kernarg_segment_size: 80
    .language:       OpenCL C
    .language_version:
      - 2
      - 0
    .max_flat_workgroup_size: 256
    .name:           _Z7gemm128ILi2ELi128EEv8GemmArgs
    .private_segment_fixed_size: 0
    .sgpr_count:     22
    .sgpr_spill_count: 0
    .symbol:         _Z7gemm128ILi2ELi128EEv8GemmArgs.kd
    .uniform_work_group_size: 1
    .uses_dynamic_stack: false
    .vgpr_count:     166
    .vgpr_spill_count: 0
    .wavefront_size: 64
  - .agpr_count:     0
    .args:
      - .offset:         0
        .size:           80
        .value_kind:     by_value
    .group_segment_fixed_size: 0
    .kernarg_segment_align: 8
    .kernarg_segment_size: 80
    .language:       OpenCL C
    .language_version:
      - 2
      - 0
    .max_flat_workgroup_size: 256
    .name:           _Z7gemm128ILi3ELi96EEv8GemmArgs
    .private_segment_fixed_size: 0
    .sgpr_count:     25
    .sgpr_spill_count: 0
    .symbol:         _Z7gemm128ILi3ELi96EEv8GemmArgs.kd
    .uniform_work_group_size: 1
    .uses_dynamic_stack: false
    .vgpr_count:     188
    .vgpr_spill_count: 0
    .wavefront_size: 64
  - .agpr_count:     0
    .args:
      - .offset:         0
        .size:           32
        .value_kind:     by_value
      - .offset:         32
        .size:           56
        .value_kind:     by_value
    .group_segment_fixed_size: 0
    .kernarg_segment_align: 8
    .kernarg_segment_size: 88
    .language:       OpenCL C
    .language_version:
      - 2
      - 0
    .max_flat_workgroup_size: 512
    .name:           _Z8gemm_bigIN3pg86EpiQKVEEvNS0_4GemmET_
    .private_segment_fixed_size: 0
    .sgpr_count:     58
    .sgpr_spill_count: 0
    .symbol:         _Z8gemm_bigIN3pg86EpiQKVEEvNS0_4GemmET_.kd
    .uniform_work_group_size: 1
    .uses_dynamic_stack: false
    .vgpr_count:     228
    .vgpr_spill_count: 0
    .wavefront_size: 64
  - .agpr_count:     0
    .args:
      - .offset:         0
        .size:           32
        .value_kind:     by_value
      - .offset:         32
        .size:           32
        .value_kind:     by_value
    .group_segment_fixed_size: 0
    .kernarg_segment_align: 8
    .kernarg_segment_size: 64
    .language:       OpenCL C
    .language_version:
      - 2
      - 0
    .max_flat_workgroup_size: 512
    .name:           _Z8gemm_bigIN3pg85EpiUPEEvNS0_4GemmET_
    .private_segment_fixed_size: 0
    .sgpr_count:     50
    .sgpr_spill_count: 0
    .symbol:         _Z8gemm_bigIN3pg85EpiUPEEvNS0_4GemmET_.kd
    .uniform_work_group_size: 1
    .uses_dynamic_stack: false
    .vgpr_count:     226
    .vgpr_spill_count: 0
    .wavefront_size: 64
